# P5: epilogue stash moved into the last K trip, wr==0 alignment barrier moved inside the epilogue (A half starts its epilogue during B's last MMA), one barrier fewer per unit
# speedup vs baseline: 1.0138x; 1.0024x over previous
; #define PG8_STAGE(bufoff, base, uoff, voff) do { _Pragma("unroll") for (int _i = 0; _i < 2; ++_i) \
;         __builtin_amdgcn_raw_ptr_buffer_load_lds((base), (PG8_LAS void*)(lds + (bufoff) + ldsw + _i * 8192), 16, (int)(voff)[_i], (int)(uoff), 0, 0); } while (0)
; #define PG8_LDA(dst, b, h) do { _Pragma("unroll") for (int m = 0; m < 4; ++m) _Pragma("unroll") for (int k = 0; k < 2; ++k) dst[m][k] = *(const PG8_LAS bf16x8*)(lds + PG8_SA(b, h) + aoff + m * 2048 + k * 1024); } while (0)
; #define PG8_LDB(dst, b, h) do { _Pragma("unroll") for (int n = 0; n < 2; ++n) _Pragma("unroll") for (int k = 0; k < 2; ++k) dst[n][k] = *(const PG8_LAS bf16x8*)(lds + PG8_SB(b, h) + boff + n * 2048 + k * 1024); } while (0)
; #define PG8_WAIT_V(n) asm volatile("s_waitcnt vmcnt(" #n ")" ::: "memory")
; #define PG8_WAIT_L(n) asm volatile("s_waitcnt lgkmcnt(" #n ")" ::: "memory")
; #define PG8_BAR __builtin_amdgcn_s_barrier()
; #define PG8_SCHED __builtin_amdgcn_sched_barrier(0)
; template <class Epi, class Sched, bool GATHER, int MODE>
; __device__ __forceinline__ void gemm_phase(PG8_LAS unsigned char* lds, PG8_LAS unsigned* scr, const Gemm g, const Sched& S, const Epi& E, int tid_in) {
;     ...
;             const unsigned a1 = cA + (unsigned)(tt + 1) * kstep;
;             const unsigned a2 = last ? nA : cA + (unsigned)(tt + 2) * kstep, b2 = last ? nB : cB + (unsigned)(tt + 2) * kstep;
;             const unsigned a3 = a2 + kstep, b3 = b2 + kstep;
;             unsigned s0[2], s1[2];
;             if (GATHER && last && has_next) { const u32x4 nx = gather_read(nxt); s0[0] = nx[0]; s0[1] = nx[1]; s1[0] = nx[2]; s1[1] = nx[3]; }
;             else { s0[0] = c0[0]; s0[1] = c0[1]; s1[0] = c1[0]; s1[1] = c1[1]; }
;             PG8_LDB(B0, 0, 0); PG8_LDB(B1, 0, 1); PG8_SCHED; PG8_LDA(At, 0, 0); PG8_STAGE(PG8_SA(1, 1), baseA, a1 + hstepA, c1);
;             PG8_WAIT_V(8); PG8_WAIT_L(0); PG8_BAR; PG8_MMA(0, 0, At, B0); PG8_MMA(0, 1, At, B1); PG8_BAR; PG8_SCHED;
;             PG8_LDA(At, 0, 1); PG8_STAGE(PG8_SB(0, 0), baseB, b2, voffB); PG8_STAGE(PG8_SB(0, 1), baseB, b2 + hstep, voffB); PG8_STAGE(PG8_SA(0, 0), baseA, a2, s0);
;             PG8_WAIT_V(8); PG8_WAIT_L(0); PG8_BAR; PG8_MMA(1, 0, At, B0); PG8_MMA(1, 1, At, B1); PG8_BAR; PG8_SCHED;
.LBB0_802:
	ds_read_b128 v[52:55], v206
	ds_read_b128 v[136:139], v206 offset:1024
	ds_read_b128 v[140:143], v206 offset:2048
	ds_read_b128 v[144:147], v206 offset:3072
	ds_read_b128 v[150:153], v207
	ds_read_b128 v[154:157], v207 offset:1024
	ds_read_b128 v[158:161], v207 offset:2048
	ds_read_b128 v[208:211], v207 offset:3072
	s_lshl_b32 s44, s43, 7
	s_add_i32 s50, s44, 0x80
	s_add_i32 s51, s44, 0x100
	s_and_b64 s[44:45], s[12:13], exec
	s_cselect_b32 s45, 0, s51
	s_add_i32 s51, s51, s41
	s_and_b64 s[12:13], s[12:13], exec
	s_cselect_b32 s13, s42, s51
	s_add_i32 s12, s45, 0x80
	s_add_i32 s44, s13, 0x80
	s_mov_b32 m0, s87
	ds_read_b128 v[212:215], v184
	ds_read_b128 v[216:219], v184 offset:1024
	ds_read_b128 v[220:223], v184 offset:2048
	ds_read_b128 v[224:227], v184 offset:3072
	ds_read_b128 v[228:231], v184 offset:4096
	ds_read_b128 v[232:235], v184 offset:5120
	ds_read_b128 v[242:245], v184 offset:6144
	ds_read_b128 v[246:249], v184 offset:7168
	buffer_load_dwordx4 v201, s[4:7], s50 offen lds
	s_mov_b32 m0, s88
	s_nop 0
	buffer_load_dwordx4 v203, s[4:7], s50 offen lds
	s_waitcnt vmcnt(8)
	s_waitcnt lgkmcnt(0)
	s_barrier
	s_setprio 1
	s_waitcnt lgkmcnt(7)
	v_mfma_i32_16x16x64_i8 v[128:131], v[52:55], v[212:215], v[128:131]
	s_waitcnt lgkmcnt(6)
	v_mfma_i32_16x16x64_i8 v[128:131], v[136:139], v[216:219], v[128:131]
	v_mfma_i32_16x16x64_i8 v[120:123], v[140:143], v[212:215], v[120:123]
	s_nop 0
	v_mfma_i32_16x16x64_i8 v[120:123], v[144:147], v[216:219], v[120:123]
	s_waitcnt lgkmcnt(5)
	v_mfma_i32_16x16x64_i8 v[112:115], v[52:55], v[220:223], v[112:115]
	s_waitcnt lgkmcnt(4)
	v_mfma_i32_16x16x64_i8 v[112:115], v[136:139], v[224:227], v[112:115]
	v_mfma_i32_16x16x64_i8 v[104:107], v[140:143], v[220:223], v[104:107]
	s_nop 0
	v_mfma_i32_16x16x64_i8 v[104:107], v[144:147], v[224:227], v[104:107]
	s_waitcnt lgkmcnt(3)
	v_mfma_i32_16x16x64_i8 v[96:99], v[52:55], v[228:231], v[96:99]
	s_waitcnt lgkmcnt(2)
	v_mfma_i32_16x16x64_i8 v[96:99], v[136:139], v[232:235], v[96:99]
	v_mfma_i32_16x16x64_i8 v[88:91], v[140:143], v[228:231], v[88:91]
	s_nop 0
	v_mfma_i32_16x16x64_i8 v[88:91], v[144:147], v[232:235], v[88:91]
	s_waitcnt lgkmcnt(1)
	v_mfma_i32_16x16x64_i8 v[80:83], v[52:55], v[242:245], v[80:83]
	s_waitcnt lgkmcnt(0)
	v_mfma_i32_16x16x64_i8 v[80:83], v[136:139], v[246:249], v[80:83]
	v_mfma_i32_16x16x64_i8 v[72:75], v[140:143], v[242:245], v[72:75]
	s_nop 0
	v_mfma_i32_16x16x64_i8 v[72:75], v[144:147], v[246:249], v[72:75]
	s_setprio 0
	s_setprio 1
	v_mfma_i32_16x16x64_i8 v[132:135], v[150:153], v[212:215], v[132:135]
	s_nop 0
	v_mfma_i32_16x16x64_i8 v[132:135], v[154:157], v[216:219], v[132:135]
	v_mfma_i32_16x16x64_i8 v[124:127], v[158:161], v[212:215], v[124:127]
	s_nop 0
	v_mfma_i32_16x16x64_i8 v[124:127], v[208:211], v[216:219], v[124:127]
	v_mfma_i32_16x16x64_i8 v[116:119], v[150:153], v[220:223], v[116:119]
	s_nop 0
	v_mfma_i32_16x16x64_i8 v[116:119], v[154:157], v[224:227], v[116:119]
	v_mfma_i32_16x16x64_i8 v[108:111], v[158:161], v[220:223], v[108:111]
	s_nop 0
	v_mfma_i32_16x16x64_i8 v[108:111], v[208:211], v[224:227], v[108:111]
	v_mfma_i32_16x16x64_i8 v[100:103], v[150:153], v[228:231], v[100:103]
	s_nop 0
	v_mfma_i32_16x16x64_i8 v[100:103], v[154:157], v[232:235], v[100:103]
	v_mfma_i32_16x16x64_i8 v[92:95], v[158:161], v[228:231], v[92:95]
	s_nop 0
	v_mfma_i32_16x16x64_i8 v[92:95], v[208:211], v[232:235], v[92:95]
	v_mfma_i32_16x16x64_i8 v[84:87], v[150:153], v[242:245], v[84:87]
	s_nop 0
	v_mfma_i32_16x16x64_i8 v[84:87], v[154:157], v[246:249], v[84:87]
	v_mfma_i32_16x16x64_i8 v[76:79], v[158:161], v[242:245], v[76:79]
	s_nop 0
	v_mfma_i32_16x16x64_i8 v[76:79], v[208:211], v[246:249], v[76:79]
	s_setprio 0
	s_barrier
	s_mov_b32 m0, s68
	s_mov_b32 s50, s6
	s_mov_b32 s51, s7
	ds_read_b128 v[212:215], v184 offset:16384
	ds_read_b128 v[216:219], v184 offset:17408
	ds_read_b128 v[220:223], v184 offset:18432
	ds_read_b128 v[224:227], v184 offset:19456
	ds_read_b128 v[228:231], v184 offset:20480
	ds_read_b128 v[232:235], v184 offset:21504
	ds_read_b128 v[242:245], v184 offset:22528
	ds_read_b128 v[246:249], v184 offset:23552
	buffer_load_dwordx4 v165, s[48:51], s13 offen lds
	s_mov_b32 m0, s69
	s_add_i32 s54, s13, 0x20000
	buffer_load_dwordx4 v180, s[48:51], s13 offen lds
	s_mov_b32 m0, s70
	s_nop 0
	buffer_load_dwordx4 v165, s[48:51], s54 offen lds
	s_mov_b32 m0, s71
	s_nop 0
	buffer_load_dwordx4 v180, s[48:51], s54 offen lds
	s_mov_b32 m0, s67
	s_nop 0
	buffer_load_dwordx4 v40, s[4:7], s45 offen lds
	s_mov_b32 m0, s72
	s_nop 0
	buffer_load_dwordx4 v41, s[4:7], s45 offen lds
	s_waitcnt vmcnt(8)
	s_waitcnt lgkmcnt(0)
	s_barrier
;     __device__ __forceinline__ void stash(const Pre2& p, PG8_LAS unsigned* scr, int t) const { scr[t] = p.a; if (t < 256) scr[512 + t] = p.b; }
; #define PG8_STAGE(bufoff, base, uoff, voff) do { _Pragma("unroll") for (int _i = 0; _i < 2; ++_i) \
;         __builtin_amdgcn_raw_ptr_buffer_load_lds((base), (PG8_LAS void*)(lds + (bufoff) + ldsw + _i * 8192), 16, (int)(voff)[_i], (int)(uoff), 0, 0); } while (0)
; #define PG8_LDA(dst, b, h) do { _Pragma("unroll") for (int m = 0; m < 4; ++m) _Pragma("unroll") for (int k = 0; k < 2; ++k) dst[m][k] = *(const PG8_LAS bf16x8*)(lds + PG8_SA(b, h) + aoff + m * 2048 + k * 1024); } while (0)
; #define PG8_LDB(dst, b, h) do { _Pragma("unroll") for (int n = 0; n < 2; ++n) _Pragma("unroll") for (int k = 0; k < 2; ++k) dst[n][k] = *(const PG8_LAS bf16x8*)(lds + PG8_SB(b, h) + boff + n * 2048 + k * 1024); } while (0)
; #define PG8_WAIT_V(n) asm volatile("s_waitcnt vmcnt(" #n ")" ::: "memory")
; #define PG8_WAIT_L(n) asm volatile("s_waitcnt lgkmcnt(" #n ")" ::: "memory")
; #define PG8_BAR __builtin_amdgcn_s_barrier()
; #define PG8_SCHED __builtin_amdgcn_sched_barrier(0)
; template <class Epi, class Sched, bool GATHER, int MODE>
; __device__ __forceinline__ void gemm_phase(PG8_LAS unsigned char* lds, PG8_LAS unsigned* scr, const Gemm g, const Sched& S, const Epi& E, int tid_in) {
;     ...
;             PG8_WAIT_V(8); PG8_WAIT_L(0); PG8_BAR; PG8_MMA(1, 0, At, B0); PG8_MMA(1, 1, At, B1); PG8_BAR; PG8_SCHED;
;             PG8_LDB(B0, 1, 0); PG8_LDB(B1, 1, 1); PG8_SCHED; PG8_LDA(At, 1, 0); PG8_STAGE(PG8_SA(0, 1), baseA, a2 + hstepA, s1);
;             PG8_WAIT_V(8); PG8_WAIT_L(0); PG8_BAR; PG8_MMA(0, 0, At, B0); PG8_MMA(0, 1, At, B1); PG8_BAR; PG8_SCHED;
;             PG8_LDA(At, 1, 1); PG8_STAGE(PG8_SB(1, 0), baseB, b3, voffB); PG8_STAGE(PG8_SB(1, 1), baseB, b3 + hstep, voffB); PG8_STAGE(PG8_SA(1, 0), baseA, a3, s0);
;     ...
;         if (Epi::HAS_PRE) { E.stash(pre, scr, tid); PG8_WAIT_L(0); PG8_BAR; }
	s_setprio 1
	s_waitcnt lgkmcnt(7)
	v_mfma_i32_16x16x64_i8 v[64:67], v[52:55], v[212:215], v[64:67]
	s_waitcnt lgkmcnt(6)
	v_mfma_i32_16x16x64_i8 v[64:67], v[136:139], v[216:219], v[64:67]
	v_mfma_i32_16x16x64_i8 v[56:59], v[140:143], v[212:215], v[56:59]
	s_nop 0
	v_mfma_i32_16x16x64_i8 v[56:59], v[144:147], v[216:219], v[56:59]
	s_waitcnt lgkmcnt(5)
	v_mfma_i32_16x16x64_i8 v[44:47], v[52:55], v[220:223], v[44:47]
	s_waitcnt lgkmcnt(4)
	v_mfma_i32_16x16x64_i8 v[44:47], v[136:139], v[224:227], v[44:47]
	v_mfma_i32_16x16x64_i8 v[32:35], v[140:143], v[220:223], v[32:35]
	s_nop 0
	v_mfma_i32_16x16x64_i8 v[32:35], v[144:147], v[224:227], v[32:35]
	s_waitcnt lgkmcnt(3)
	v_mfma_i32_16x16x64_i8 v[24:27], v[52:55], v[228:231], v[24:27]
	s_waitcnt lgkmcnt(2)
	v_mfma_i32_16x16x64_i8 v[24:27], v[136:139], v[232:235], v[24:27]
	v_mfma_i32_16x16x64_i8 v[16:19], v[140:143], v[228:231], v[16:19]
	s_nop 0
	v_mfma_i32_16x16x64_i8 v[16:19], v[144:147], v[232:235], v[16:19]
	s_waitcnt lgkmcnt(1)
	v_mfma_i32_16x16x64_i8 v[8:11], v[52:55], v[242:245], v[8:11]
	s_waitcnt lgkmcnt(0)
	v_mfma_i32_16x16x64_i8 v[8:11], v[136:139], v[246:249], v[8:11]
	v_mfma_i32_16x16x64_i8 v[0:3], v[140:143], v[242:245], v[0:3]
	s_nop 0
	v_mfma_i32_16x16x64_i8 v[0:3], v[144:147], v[246:249], v[0:3]
	s_setprio 0
	s_setprio 1
	v_mfma_i32_16x16x64_i8 v[68:71], v[150:153], v[212:215], v[68:71]
	s_nop 0
	v_mfma_i32_16x16x64_i8 v[68:71], v[154:157], v[216:219], v[68:71]
	v_mfma_i32_16x16x64_i8 v[60:63], v[158:161], v[212:215], v[60:63]
	s_nop 0
	v_mfma_i32_16x16x64_i8 v[60:63], v[208:211], v[216:219], v[60:63]
	v_mfma_i32_16x16x64_i8 v[48:51], v[150:153], v[220:223], v[48:51]
	s_nop 0
	v_mfma_i32_16x16x64_i8 v[48:51], v[154:157], v[224:227], v[48:51]
	v_mfma_i32_16x16x64_i8 v[36:39], v[158:161], v[220:223], v[36:39]
	s_nop 0
	v_mfma_i32_16x16x64_i8 v[36:39], v[208:211], v[224:227], v[36:39]
	v_mfma_i32_16x16x64_i8 v[28:31], v[150:153], v[228:231], v[28:31]
	s_nop 0
	v_mfma_i32_16x16x64_i8 v[28:31], v[154:157], v[232:235], v[28:31]
	v_mfma_i32_16x16x64_i8 v[20:23], v[158:161], v[228:231], v[20:23]
	s_nop 0
	v_mfma_i32_16x16x64_i8 v[20:23], v[208:211], v[232:235], v[20:23]
	v_mfma_i32_16x16x64_i8 v[12:15], v[150:153], v[242:245], v[12:15]
	s_nop 0
	v_mfma_i32_16x16x64_i8 v[12:15], v[154:157], v[246:249], v[12:15]
	v_mfma_i32_16x16x64_i8 v[4:7], v[158:161], v[242:245], v[4:7]
	s_nop 0
	v_mfma_i32_16x16x64_i8 v[4:7], v[208:211], v[246:249], v[4:7]
	s_setprio 0
	s_barrier
	ds_read_b128 v[52:55], v148
	ds_read_b128 v[136:139], v148 offset:1024
	ds_read_b128 v[140:143], v148 offset:2048
	ds_read_b128 v[144:147], v148 offset:3072
	ds_read_b128 v[150:153], v149
	ds_read_b128 v[154:157], v149 offset:1024
	ds_read_b128 v[158:161], v149 offset:2048
	ds_read_b128 v[208:211], v149 offset:3072
	s_mov_b32 m0, s73
	ds_read_b128 v[212:215], v184 offset:32768
	ds_read_b128 v[216:219], v184 offset:33792
	ds_read_b128 v[220:223], v184 offset:34816
	ds_read_b128 v[224:227], v184 offset:35840
	ds_read_b128 v[228:231], v184 offset:36864
	ds_read_b128 v[232:235], v184 offset:37888
	ds_read_b128 v[242:245], v184 offset:38912
	ds_read_b128 v[246:249], v184 offset:39936
	buffer_load_dwordx4 v42, s[4:7], s45 offen lds
	s_mov_b32 m0, s74
	s_nop 0
	buffer_load_dwordx4 v43, s[4:7], s45 offen lds
	s_waitcnt vmcnt(8)
	s_waitcnt lgkmcnt(0)
	s_barrier
	s_setprio 1
	s_waitcnt lgkmcnt(7)
	v_mfma_i32_16x16x64_i8 v[128:131], v[52:55], v[212:215], v[128:131]
	s_waitcnt lgkmcnt(6)
	v_mfma_i32_16x16x64_i8 v[128:131], v[136:139], v[216:219], v[128:131]
	v_mfma_i32_16x16x64_i8 v[120:123], v[140:143], v[212:215], v[120:123]
	s_nop 0
	v_mfma_i32_16x16x64_i8 v[120:123], v[144:147], v[216:219], v[120:123]
	s_waitcnt lgkmcnt(5)
	v_mfma_i32_16x16x64_i8 v[112:115], v[52:55], v[220:223], v[112:115]
	s_waitcnt lgkmcnt(4)
	v_mfma_i32_16x16x64_i8 v[112:115], v[136:139], v[224:227], v[112:115]
	v_mfma_i32_16x16x64_i8 v[104:107], v[140:143], v[220:223], v[104:107]
	s_nop 0
	v_mfma_i32_16x16x64_i8 v[104:107], v[144:147], v[224:227], v[104:107]
	s_waitcnt lgkmcnt(3)
	v_mfma_i32_16x16x64_i8 v[96:99], v[52:55], v[228:231], v[96:99]
	s_waitcnt lgkmcnt(2)
	v_mfma_i32_16x16x64_i8 v[96:99], v[136:139], v[232:235], v[96:99]
	v_mfma_i32_16x16x64_i8 v[88:91], v[140:143], v[228:231], v[88:91]
	s_nop 0
	v_mfma_i32_16x16x64_i8 v[88:91], v[144:147], v[232:235], v[88:91]
	s_waitcnt lgkmcnt(1)
	v_mfma_i32_16x16x64_i8 v[80:83], v[52:55], v[242:245], v[80:83]
	s_waitcnt lgkmcnt(0)
	v_mfma_i32_16x16x64_i8 v[80:83], v[136:139], v[246:249], v[80:83]
	v_mfma_i32_16x16x64_i8 v[72:75], v[140:143], v[242:245], v[72:75]
	s_nop 0
	v_mfma_i32_16x16x64_i8 v[72:75], v[144:147], v[246:249], v[72:75]
	s_setprio 0
	s_setprio 1
	v_mfma_i32_16x16x64_i8 v[132:135], v[150:153], v[212:215], v[132:135]
	s_nop 0
	v_mfma_i32_16x16x64_i8 v[132:135], v[154:157], v[216:219], v[132:135]
	v_mfma_i32_16x16x64_i8 v[124:127], v[158:161], v[212:215], v[124:127]
	s_nop 0
	v_mfma_i32_16x16x64_i8 v[124:127], v[208:211], v[216:219], v[124:127]
	v_mfma_i32_16x16x64_i8 v[116:119], v[150:153], v[220:223], v[116:119]
	s_nop 0
	v_mfma_i32_16x16x64_i8 v[116:119], v[154:157], v[224:227], v[116:119]
	v_mfma_i32_16x16x64_i8 v[108:111], v[158:161], v[220:223], v[108:111]
	s_nop 0
	v_mfma_i32_16x16x64_i8 v[108:111], v[208:211], v[224:227], v[108:111]
	v_mfma_i32_16x16x64_i8 v[100:103], v[150:153], v[228:231], v[100:103]
	s_nop 0
	v_mfma_i32_16x16x64_i8 v[100:103], v[154:157], v[232:235], v[100:103]
	v_mfma_i32_16x16x64_i8 v[92:95], v[158:161], v[228:231], v[92:95]
	s_nop 0
	v_mfma_i32_16x16x64_i8 v[92:95], v[208:211], v[232:235], v[92:95]
	v_mfma_i32_16x16x64_i8 v[84:87], v[150:153], v[242:245], v[84:87]
	s_nop 0
	v_mfma_i32_16x16x64_i8 v[84:87], v[154:157], v[246:249], v[84:87]
	v_mfma_i32_16x16x64_i8 v[76:79], v[158:161], v[242:245], v[76:79]
	s_nop 0
	v_mfma_i32_16x16x64_i8 v[76:79], v[208:211], v[246:249], v[76:79]
	s_setprio 0
	s_barrier
	s_cmp_eq_u32 s43, 6
	s_cbranch_scc0 .Lp5_nostash
	ds_write_b32 v182, v205
	s_and_saveexec_b64 s[98:99], s[34:35]
	ds_write_b32 v182, v204 offset:2048
	s_or_b64 exec, exec, s[98:99]
; #define PG8_STAGE(bufoff, base, uoff, voff) do { _Pragma("unroll") for (int _i = 0; _i < 2; ++_i) \
;         __builtin_amdgcn_raw_ptr_buffer_load_lds((base), (PG8_LAS void*)(lds + (bufoff) + ldsw + _i * 8192), 16, (int)(voff)[_i], (int)(uoff), 0, 0); } while (0)
; #define PG8_LDA(dst, b, h) do { _Pragma("unroll") for (int m = 0; m < 4; ++m) _Pragma("unroll") for (int k = 0; k < 2; ++k) dst[m][k] = *(const PG8_LAS bf16x8*)(lds + PG8_SA(b, h) + aoff + m * 2048 + k * 1024); } while (0)
; #define PG8_WAIT_V(n) asm volatile("s_waitcnt vmcnt(" #n ")" ::: "memory")
; #define PG8_WAIT_L(n) asm volatile("s_waitcnt lgkmcnt(" #n ")" ::: "memory")
; #define PG8_BAR __builtin_amdgcn_s_barrier()
; #define PG8_SCHED __builtin_amdgcn_sched_barrier(0)
; template <class Epi, class Sched, bool GATHER, int MODE>
; __device__ __forceinline__ void gemm_phase(PG8_LAS unsigned char* lds, PG8_LAS unsigned* scr, const Gemm g, const Sched& S, const Epi& E, int tid_in) {
;     ...
;             PG8_LDA(At, 1, 1); PG8_STAGE(PG8_SB(1, 0), baseB, b3, voffB); PG8_STAGE(PG8_SB(1, 1), baseB, b3 + hstep, voffB); PG8_STAGE(PG8_SA(1, 0), baseA, a3, s0);
;             PG8_WAIT_V(8); PG8_WAIT_L(0); PG8_BAR; PG8_MMA(1, 0, At, B0); PG8_MMA(1, 1, At, B1); PG8_BAR; PG8_SCHED;
;         }
.Lp5_nostash:
	s_mov_b32 m0, s81
	ds_read_b128 v[212:215], v184 offset:49152
	ds_read_b128 v[216:219], v184 offset:50176
	ds_read_b128 v[220:223], v184 offset:51200
	ds_read_b128 v[224:227], v184 offset:52224
	ds_read_b128 v[228:231], v184 offset:53248
	ds_read_b128 v[232:235], v184 offset:54272
	ds_read_b128 v[242:245], v184 offset:55296
	ds_read_b128 v[246:249], v184 offset:56320
	buffer_load_dwordx4 v165, s[48:51], s44 offen lds
	s_mov_b32 m0, s82
	s_add_i32 s13, s13, 0x20080
	buffer_load_dwordx4 v180, s[48:51], s44 offen lds
	s_mov_b32 m0, s85
	s_nop 0
	buffer_load_dwordx4 v165, s[48:51], s13 offen lds
	s_mov_b32 m0, s86
	s_nop 0
	buffer_load_dwordx4 v180, s[48:51], s13 offen lds
	s_mov_b32 m0, s83
	s_nop 0
	buffer_load_dwordx4 v40, s[4:7], s12 offen lds
	s_mov_b32 m0, s84
	s_nop 0
	buffer_load_dwordx4 v41, s[4:7], s12 offen lds
	s_waitcnt vmcnt(8)
	s_waitcnt lgkmcnt(0)
	s_barrier
	s_setprio 1
	s_waitcnt lgkmcnt(7)
	v_mfma_i32_16x16x64_i8 v[64:67], v[52:55], v[212:215], v[64:67]
	s_waitcnt lgkmcnt(6)
	v_mfma_i32_16x16x64_i8 v[64:67], v[136:139], v[216:219], v[64:67]
	v_mfma_i32_16x16x64_i8 v[56:59], v[140:143], v[212:215], v[56:59]
	s_nop 0
	v_mfma_i32_16x16x64_i8 v[56:59], v[144:147], v[216:219], v[56:59]
	s_waitcnt lgkmcnt(5)
	v_mfma_i32_16x16x64_i8 v[44:47], v[52:55], v[220:223], v[44:47]
	s_waitcnt lgkmcnt(4)
	v_mfma_i32_16x16x64_i8 v[44:47], v[136:139], v[224:227], v[44:47]
	v_mfma_i32_16x16x64_i8 v[32:35], v[140:143], v[220:223], v[32:35]
	s_nop 0
	v_mfma_i32_16x16x64_i8 v[32:35], v[144:147], v[224:227], v[32:35]
	s_waitcnt lgkmcnt(3)
	v_mfma_i32_16x16x64_i8 v[24:27], v[52:55], v[228:231], v[24:27]
	s_waitcnt lgkmcnt(2)
	v_mfma_i32_16x16x64_i8 v[24:27], v[136:139], v[232:235], v[24:27]
	v_mfma_i32_16x16x64_i8 v[16:19], v[140:143], v[228:231], v[16:19]
	s_nop 0
	v_mfma_i32_16x16x64_i8 v[16:19], v[144:147], v[232:235], v[16:19]
	s_waitcnt lgkmcnt(1)
	v_mfma_i32_16x16x64_i8 v[8:11], v[52:55], v[242:245], v[8:11]
	s_waitcnt lgkmcnt(0)
	v_mfma_i32_16x16x64_i8 v[8:11], v[136:139], v[246:249], v[8:11]
	v_mfma_i32_16x16x64_i8 v[0:3], v[140:143], v[242:245], v[0:3]
	s_nop 0
	v_mfma_i32_16x16x64_i8 v[0:3], v[144:147], v[246:249], v[0:3]
	s_setprio 0
	s_setprio 1
	v_mfma_i32_16x16x64_i8 v[68:71], v[150:153], v[212:215], v[68:71]
	s_nop 0
	v_mfma_i32_16x16x64_i8 v[68:71], v[154:157], v[216:219], v[68:71]
	v_mfma_i32_16x16x64_i8 v[60:63], v[158:161], v[212:215], v[60:63]
	s_nop 0
	v_mfma_i32_16x16x64_i8 v[60:63], v[208:211], v[216:219], v[60:63]
	v_mfma_i32_16x16x64_i8 v[48:51], v[150:153], v[220:223], v[48:51]
	s_nop 0
	v_mfma_i32_16x16x64_i8 v[48:51], v[154:157], v[224:227], v[48:51]
	v_mfma_i32_16x16x64_i8 v[36:39], v[158:161], v[220:223], v[36:39]
	s_nop 0
	v_mfma_i32_16x16x64_i8 v[36:39], v[208:211], v[224:227], v[36:39]
	v_mfma_i32_16x16x64_i8 v[28:31], v[150:153], v[228:231], v[28:31]
	s_nop 0
	v_mfma_i32_16x16x64_i8 v[28:31], v[154:157], v[232:235], v[28:31]
	v_mfma_i32_16x16x64_i8 v[20:23], v[158:161], v[228:231], v[20:23]
	s_nop 0
	v_mfma_i32_16x16x64_i8 v[20:23], v[208:211], v[232:235], v[20:23]
	v_mfma_i32_16x16x64_i8 v[12:15], v[150:153], v[242:245], v[12:15]
	s_nop 0
	v_mfma_i32_16x16x64_i8 v[12:15], v[154:157], v[246:249], v[12:15]
	v_mfma_i32_16x16x64_i8 v[4:7], v[158:161], v[242:245], v[4:7]
	s_nop 0
	v_mfma_i32_16x16x64_i8 v[4:7], v[208:211], v[246:249], v[4:7]
	s_setprio 0
	s_barrier
	s_cmp_gt_u32 s43, 5
	s_cbranch_scc1 .LBB0_805

; #define PG8_LAS __attribute__((address_space(3)))
; #define PG8_BAR __builtin_amdgcn_s_barrier()
;     __device__ __forceinline__ void operator()(const i32x4 (&acc)[2][2][4][2], const Unit& u, int wr, int wc, int fr, int fq, PG8_LAS unsigned* scr) const {
;         const int j = u.pn & 7;
;         const int row0 = u.pm * BM + wr * 64 + fr, c0 = j * 128 + wc * 32 + 8 * fq, cl = wc * 32 + 8 * fq;
;         f32x4 bgv[2], buv[2], csg[2], csu[2];
;         constexpr float C2 = 1.702f * 1.44269504f;
; #pragma unroll
;         for (int n = 0; n < 2; ++n) { bgv[n] = *(const PG8_LAS f32x4*)(scr + 512 + cl + 4 * n) * C2; buv[n] = *(const PG8_LAS f32x4*)(scr + 512 + 128 + cl + 4 * n);
;             csg[n] = *(const PG8_LAS f32x4*)(scr + 256 + cl + 4 * n) * (C2 / 127.0f); csu[n] = *(const PG8_LAS f32x4*)(scr + 256 + 128 + cl + 4 * n) * (1.0f / 127.0f); }
; #pragma unroll
;         for (int ai = 0; ai < 2; ++ai)
; #pragma unroll
;             for (int mp = 0; mp < 4; mp += 2) { unsigned wp[2][2];
; #pragma unroll
;                 for (int hm = 0; hm < 2; ++hm) { const int m = mp + hm; const int r = ai * HALF + wr * 64 + m * 16 + fr; const float rs = __uint_as_float(scr[r]); float o[8];
; #pragma unroll
;                     for (int n = 0; n < 2; ++n) { const f32x4 sgr = csg[n] * rs, sur = csu[n] * rs;
; #pragma unroll
;                         for (int q = 0; q < 4; ++q) { const float h = fminf(__builtin_fmaf((float)acc[ai][0][m][n][q], sgr[q], bgv[n][q]), 7.0f * C2), up = fminf(fmaxf(__builtin_fmaf((float)acc[ai][1][m][n][q], sur[q], buv[n][q]), -7.0f), 7.0f);
;                             const float sg = __builtin_amdgcn_rcpf(1.0f + __builtin_amdgcn_exp2f(-h)); o[4 * n + q] = __builtin_fmaf(up, ACT_SC / C2, ACT_SC / C2) * (h * sg); } }
;                     int w0 = __builtin_amdgcn_cvt_pk_fp8_f32(o[0], o[1], 0, false); w0 = __builtin_amdgcn_cvt_pk_fp8_f32(o[2], o[3], w0, true);
;                     int w1 = __builtin_amdgcn_cvt_pk_fp8_f32(o[4], o[5], 0, false); w1 = __builtin_amdgcn_cvt_pk_fp8_f32(o[6], o[7], w1, true);
;                     wp[hm][0] = (unsigned)w0; wp[hm][1] = (unsigned)w1; }
; template <class Epi, class Sched, bool GATHER, int MODE>
; __device__ __forceinline__ void gemm_phase(PG8_LAS unsigned char* lds, PG8_LAS unsigned* scr, const Gemm g, const Sched& S, const Epi& E, int tid_in) {
;     ...
;         if (wr == 0) PG8_BAR;
.LBB0_807:
	v_ashrrev_i32_e32 v185, 2, v168
	v_and_b32_e32 v185, 0xffffffc0, v185
	v_bfe_u32 v201, v168, 4, 2
	v_lshrrev_b32_e32 v208, 1, v168
	v_and_b32_e32 v208, 0x60, v208
	v_lshl_or_b32 v208, v201, 3, v208
	s_lshl_b32 s10, s39, 7
	s_and_b32 s10, s10, 0x380
	v_and_b32_e32 v201, 1, v201
	v_lshlrev_b32_e32 v207, 3, v201
	v_add_u32_e32 v206, s10, v208
	v_sub_u32_e32 v206, v206, v207
	v_mov_b32_e32 v207, 0
	v_lshlrev_b32_e32 v201, 4, v201
	v_lshlrev_b32_e32 v208, 2, v208
	v_readlane_b32 s10, v255, 5
	v_and_b32_e32 v160, 15, v168
	v_lshl_add_u32 v161, v185, 2, 0
	v_lshl_add_u32 v161, v160, 2, v161
	v_add_u32_e32 v161, s10, v161
	ds_read2_b32 v[152:153], v161 offset0:0 offset1:16
	ds_read2_b32 v[154:155], v161 offset0:32 offset1:48
	ds_read2_b32 v[156:157], v161 offset0:128 offset1:144
	ds_read2_b32 v[158:159], v161 offset0:160 offset1:176
	v_lshl_add_u32 v185, s40, 8, v185
	v_or_b32_e32 v185, v185, v160
	v_add_u32_e32 v185, v185, v201
	s_mov_b32 s100, 0x405083aa
	s_mov_b32 s101, 0x405083aa
	v_add_u32_e32 v160, 0x21100, v208
	ds_read_b128 v[136:139], v160
	v_add_u32_e32 v160, 0x21300, v208
	ds_read_b128 v[140:143], v160
	v_add_u32_e32 v160, 0x20d00, v208
	ds_read_b128 v[144:147], v160
	v_add_u32_e32 v160, 0x20f00, v208
	ds_read_b128 v[148:151], v160
	s_waitcnt lgkmcnt(0)
	v_mul_f32_e32 v136, 0x401d265f, v136
	v_mul_f32_e32 v137, 0x401d265f, v137
	v_mul_f32_e32 v138, 0x401d265f, v138
	v_mul_f32_e32 v139, 0x401d265f, v139
	v_mul_f32_e32 v144, 0x3c9e6325, v144
	v_mul_f32_e32 v145, 0x3c9e6325, v145
	v_mul_f32_e32 v146, 0x3c9e6325, v146
	v_mul_f32_e32 v147, 0x3c9e6325, v147
	v_mul_f32_e32 v148, 0x3c010204, v148
	v_mul_f32_e32 v149, 0x3c010204, v149
	v_mul_f32_e32 v150, 0x3c010204, v150
	v_mul_f32_e32 v151, 0x3c010204, v151
	v_cvt_f32_i32_e32 v128, v128
	v_cvt_f32_i32_e32 v129, v129
	v_cvt_f32_i32_e32 v130, v130
	v_cvt_f32_i32_e32 v131, v131
	v_cvt_f32_i32_e32 v132, v132
	v_cvt_f32_i32_e32 v133, v133
	v_cvt_f32_i32_e32 v134, v134
	v_cvt_f32_i32_e32 v135, v135
	v_pk_mul_f32 v[160:161], v[144:145], v[152:153] op_sel_hi:[1,0]
	v_pk_mul_f32 v[162:163], v[146:147], v[152:153] op_sel_hi:[1,0]
	v_pk_fma_f32 v[128:129], v[128:129], v[160:161], v[136:137]
	v_pk_fma_f32 v[130:131], v[130:131], v[162:163], v[138:139]
	v_pk_mul_f32 v[160:161], v[148:149], v[152:153] op_sel_hi:[1,0]
	v_pk_mul_f32 v[162:163], v[150:151], v[152:153] op_sel_hi:[1,0]
	v_min_f32_e32 v128, 0x41898193, v128
	v_min_f32_e32 v129, 0x41898193, v129
	v_min_f32_e32 v130, 0x41898193, v130
	v_min_f32_e32 v131, 0x41898193, v131
	v_pk_fma_f32 v[132:133], v[132:133], v[160:161], v[140:141]
	v_pk_fma_f32 v[134:135], v[134:135], v[162:163], v[142:143]
	v_exp_f32_e64 v160, -v128
	v_exp_f32_e64 v161, -v129
	v_exp_f32_e64 v162, -v130
	v_exp_f32_e64 v163, -v131
	v_med3_f32 v132, v132, s8, v199
	v_med3_f32 v133, v133, s8, v199
	v_med3_f32 v134, v134, s8, v199
	v_med3_f32 v135, v135, s8, v199
	v_pk_add_f32 v[160:161], v[160:161], 1.0 op_sel_hi:[1,0]
	v_pk_add_f32 v[162:163], v[162:163], 1.0 op_sel_hi:[1,0]
	v_pk_fma_f32 v[132:133], v[132:133], s[100:101], s[100:101]
	v_pk_fma_f32 v[134:135], v[134:135], s[100:101], s[100:101]
	v_rcp_f32_e32 v160, v160
	v_rcp_f32_e32 v161, v161
	v_rcp_f32_e32 v162, v162
	v_rcp_f32_e32 v163, v163
	v_nop
	v_pk_mul_f32 v[128:129], v[128:129], v[160:161]
	v_pk_mul_f32 v[130:131], v[130:131], v[162:163]
	v_pk_mul_f32 v[128:129], v[132:133], v[128:129]
	v_pk_mul_f32 v[130:131], v[134:135], v[130:131]
	v_cvt_pk_fp8_f32 v128, v128, v129
	v_cvt_pk_fp8_f32 v128, v130, v131 op_sel:[0,0,1]
	v_cvt_f32_i32_e32 v112, v112
	v_cvt_f32_i32_e32 v113, v113
	v_cvt_f32_i32_e32 v114, v114
	v_cvt_f32_i32_e32 v115, v115
	v_cvt_f32_i32_e32 v116, v116
	v_cvt_f32_i32_e32 v117, v117
	v_cvt_f32_i32_e32 v118, v118
	v_cvt_f32_i32_e32 v119, v119
	v_pk_mul_f32 v[202:203], v[144:145], v[152:153] op_sel:[0,1] op_sel_hi:[1,1]
	v_pk_mul_f32 v[204:205], v[146:147], v[152:153] op_sel:[0,1] op_sel_hi:[1,1]
	v_pk_fma_f32 v[112:113], v[112:113], v[202:203], v[136:137]
	v_pk_fma_f32 v[114:115], v[114:115], v[204:205], v[138:139]
	v_pk_mul_f32 v[202:203], v[148:149], v[152:153] op_sel:[0,1] op_sel_hi:[1,1]
	v_pk_mul_f32 v[204:205], v[150:151], v[152:153] op_sel:[0,1] op_sel_hi:[1,1]
	v_min_f32_e32 v112, 0x41898193, v112
	v_min_f32_e32 v113, 0x41898193, v113
	v_min_f32_e32 v114, 0x41898193, v114
	v_min_f32_e32 v115, 0x41898193, v115
	v_pk_fma_f32 v[116:117], v[116:117], v[202:203], v[140:141]
	v_pk_fma_f32 v[118:119], v[118:119], v[204:205], v[142:143]
	v_exp_f32_e64 v202, -v112
	v_exp_f32_e64 v203, -v113
	v_exp_f32_e64 v204, -v114
	v_exp_f32_e64 v205, -v115
	v_med3_f32 v116, v116, s8, v199
	v_med3_f32 v117, v117, s8, v199
	v_med3_f32 v118, v118, s8, v199
	v_med3_f32 v119, v119, s8, v199
	v_pk_add_f32 v[202:203], v[202:203], 1.0 op_sel_hi:[1,0]
	v_pk_add_f32 v[204:205], v[204:205], 1.0 op_sel_hi:[1,0]
	v_pk_fma_f32 v[116:117], v[116:117], s[100:101], s[100:101]
	v_pk_fma_f32 v[118:119], v[118:119], s[100:101], s[100:101]
	v_rcp_f32_e32 v202, v202
	v_rcp_f32_e32 v203, v203
	v_rcp_f32_e32 v204, v204
	v_rcp_f32_e32 v205, v205
	v_nop
	v_pk_mul_f32 v[112:113], v[112:113], v[202:203]
	v_pk_mul_f32 v[114:115], v[114:115], v[204:205]
	v_pk_mul_f32 v[112:113], v[116:117], v[112:113]
	v_pk_mul_f32 v[114:115], v[118:119], v[114:115]
	v_cvt_pk_fp8_f32 v130, v112, v113
	v_cvt_pk_fp8_f32 v130, v114, v115 op_sel:[0,0,1]
	s_and_b64 vcc, exec, s[62:63]
	s_cbranch_vccz .Lp5_epi_nobar
	s_barrier
;     __device__ __forceinline__ void operator()(const i32x4 (&acc)[2][2][4][2], const Unit& u, int wr, int wc, int fr, int fq, PG8_LAS unsigned* scr) const {
;     ...
;                 for (int hm = 0; hm < 2; ++hm) { const int m = mp + hm; const int r = ai * HALF + wr * 64 + m * 16 + fr; const float rs = __uint_as_float(scr[r]); float o[8];
; #pragma unroll
;                     for (int n = 0; n < 2; ++n) { const f32x4 sgr = csg[n] * rs, sur = csu[n] * rs;
; #pragma unroll
;                         for (int q = 0; q < 4; ++q) { const float h = fminf(__builtin_fmaf((float)acc[ai][0][m][n][q], sgr[q], bgv[n][q]), 7.0f * C2), up = fminf(fmaxf(__builtin_fmaf((float)acc[ai][1][m][n][q], sur[q], buv[n][q]), -7.0f), 7.0f);
;                             const float sg = __builtin_amdgcn_rcpf(1.0f + __builtin_amdgcn_exp2f(-h)); o[4 * n + q] = __builtin_fmaf(up, ACT_SC / C2, ACT_SC / C2) * (h * sg); } }
;                     int w0 = __builtin_amdgcn_cvt_pk_fp8_f32(o[0], o[1], 0, false); w0 = __builtin_amdgcn_cvt_pk_fp8_f32(o[2], o[3], w0, true);
;                     int w1 = __builtin_amdgcn_cvt_pk_fp8_f32(o[4], o[5], 0, false); w1 = __builtin_amdgcn_cvt_pk_fp8_f32(o[6], o[7], w1, true);
;                     wp[hm][0] = (unsigned)w0; wp[hm][1] = (unsigned)w1; }
.Lp5_epi_nobar:
	v_cvt_f32_i32_e32 v96, v96
	v_cvt_f32_i32_e32 v97, v97
	v_cvt_f32_i32_e32 v98, v98
	v_cvt_f32_i32_e32 v99, v99
	v_cvt_f32_i32_e32 v100, v100
	v_cvt_f32_i32_e32 v101, v101
	v_cvt_f32_i32_e32 v102, v102
	v_cvt_f32_i32_e32 v103, v103
	v_pk_mul_f32 v[160:161], v[144:145], v[154:155] op_sel_hi:[1,0]
	v_pk_mul_f32 v[162:163], v[146:147], v[154:155] op_sel_hi:[1,0]
	v_pk_fma_f32 v[96:97], v[96:97], v[160:161], v[136:137]
	v_pk_fma_f32 v[98:99], v[98:99], v[162:163], v[138:139]
	v_pk_mul_f32 v[160:161], v[148:149], v[154:155] op_sel_hi:[1,0]
	v_pk_mul_f32 v[162:163], v[150:151], v[154:155] op_sel_hi:[1,0]
	v_min_f32_e32 v96, 0x41898193, v96
	v_min_f32_e32 v97, 0x41898193, v97
	v_min_f32_e32 v98, 0x41898193, v98
	v_min_f32_e32 v99, 0x41898193, v99
	v_pk_fma_f32 v[100:101], v[100:101], v[160:161], v[140:141]
	v_pk_fma_f32 v[102:103], v[102:103], v[162:163], v[142:143]
	v_exp_f32_e64 v160, -v96
	v_exp_f32_e64 v161, -v97
	v_exp_f32_e64 v162, -v98
	v_exp_f32_e64 v163, -v99
	v_med3_f32 v100, v100, s8, v199
	v_med3_f32 v101, v101, s8, v199
	v_med3_f32 v102, v102, s8, v199
	v_med3_f32 v103, v103, s8, v199
	v_pk_add_f32 v[160:161], v[160:161], 1.0 op_sel_hi:[1,0]
	v_pk_add_f32 v[162:163], v[162:163], 1.0 op_sel_hi:[1,0]
	v_pk_fma_f32 v[100:101], v[100:101], s[100:101], s[100:101]
	v_pk_fma_f32 v[102:103], v[102:103], s[100:101], s[100:101]
	v_rcp_f32_e32 v160, v160
	v_rcp_f32_e32 v161, v161
	v_rcp_f32_e32 v162, v162
	v_rcp_f32_e32 v163, v163
	v_nop
	v_pk_mul_f32 v[96:97], v[96:97], v[160:161]
	v_pk_mul_f32 v[98:99], v[98:99], v[162:163]
	v_pk_mul_f32 v[96:97], v[100:101], v[96:97]
	v_pk_mul_f32 v[98:99], v[102:103], v[98:99]
	v_cvt_pk_fp8_f32 v96, v96, v97
	v_cvt_pk_fp8_f32 v96, v98, v99 op_sel:[0,0,1]
	v_cvt_f32_i32_e32 v80, v80
	v_cvt_f32_i32_e32 v81, v81
	v_cvt_f32_i32_e32 v82, v82
	v_cvt_f32_i32_e32 v83, v83
	v_cvt_f32_i32_e32 v84, v84
	v_cvt_f32_i32_e32 v85, v85
	v_cvt_f32_i32_e32 v86, v86
	v_cvt_f32_i32_e32 v87, v87
	v_pk_mul_f32 v[202:203], v[144:145], v[154:155] op_sel:[0,1] op_sel_hi:[1,1]
	v_pk_mul_f32 v[204:205], v[146:147], v[154:155] op_sel:[0,1] op_sel_hi:[1,1]
	v_pk_fma_f32 v[80:81], v[80:81], v[202:203], v[136:137]
	v_pk_fma_f32 v[82:83], v[82:83], v[204:205], v[138:139]
	v_pk_mul_f32 v[202:203], v[148:149], v[154:155] op_sel:[0,1] op_sel_hi:[1,1]
	v_pk_mul_f32 v[204:205], v[150:151], v[154:155] op_sel:[0,1] op_sel_hi:[1,1]
	v_min_f32_e32 v80, 0x41898193, v80
	v_min_f32_e32 v81, 0x41898193, v81
	v_min_f32_e32 v82, 0x41898193, v82
	v_min_f32_e32 v83, 0x41898193, v83
	v_pk_fma_f32 v[84:85], v[84:85], v[202:203], v[140:141]
	v_pk_fma_f32 v[86:87], v[86:87], v[204:205], v[142:143]
	v_exp_f32_e64 v202, -v80
	v_exp_f32_e64 v203, -v81
	v_exp_f32_e64 v204, -v82
	v_exp_f32_e64 v205, -v83
	v_med3_f32 v84, v84, s8, v199
	v_med3_f32 v85, v85, s8, v199
	v_med3_f32 v86, v86, s8, v199
	v_med3_f32 v87, v87, s8, v199
	v_pk_add_f32 v[202:203], v[202:203], 1.0 op_sel_hi:[1,0]
	v_pk_add_f32 v[204:205], v[204:205], 1.0 op_sel_hi:[1,0]
	v_pk_fma_f32 v[84:85], v[84:85], s[100:101], s[100:101]
	v_pk_fma_f32 v[86:87], v[86:87], s[100:101], s[100:101]
	v_rcp_f32_e32 v202, v202
	v_rcp_f32_e32 v203, v203
	v_rcp_f32_e32 v204, v204
	v_rcp_f32_e32 v205, v205
	v_nop
	v_pk_mul_f32 v[80:81], v[80:81], v[202:203]
	v_pk_mul_f32 v[82:83], v[82:83], v[204:205]
	v_pk_mul_f32 v[80:81], v[84:85], v[80:81]
	v_pk_mul_f32 v[82:83], v[86:87], v[82:83]
	v_cvt_pk_fp8_f32 v98, v80, v81
	v_cvt_pk_fp8_f32 v98, v82, v83 op_sel:[0,0,1]
	v_cvt_f32_i32_e32 v64, v64
	v_cvt_f32_i32_e32 v65, v65
	v_cvt_f32_i32_e32 v66, v66
	v_cvt_f32_i32_e32 v67, v67
	v_cvt_f32_i32_e32 v68, v68
	v_cvt_f32_i32_e32 v69, v69
	v_cvt_f32_i32_e32 v70, v70
	v_cvt_f32_i32_e32 v71, v71
	v_pk_mul_f32 v[160:161], v[144:145], v[156:157] op_sel_hi:[1,0]
	v_pk_mul_f32 v[162:163], v[146:147], v[156:157] op_sel_hi:[1,0]
	v_pk_fma_f32 v[64:65], v[64:65], v[160:161], v[136:137]
	v_pk_fma_f32 v[66:67], v[66:67], v[162:163], v[138:139]
	v_pk_mul_f32 v[160:161], v[148:149], v[156:157] op_sel_hi:[1,0]
	v_pk_mul_f32 v[162:163], v[150:151], v[156:157] op_sel_hi:[1,0]
	v_min_f32_e32 v64, 0x41898193, v64
	v_min_f32_e32 v65, 0x41898193, v65
	v_min_f32_e32 v66, 0x41898193, v66
	v_min_f32_e32 v67, 0x41898193, v67
	v_pk_fma_f32 v[68:69], v[68:69], v[160:161], v[140:141]
	v_pk_fma_f32 v[70:71], v[70:71], v[162:163], v[142:143]
	v_exp_f32_e64 v160, -v64
	v_exp_f32_e64 v161, -v65
	v_exp_f32_e64 v162, -v66
	v_exp_f32_e64 v163, -v67
	v_med3_f32 v68, v68, s8, v199
	v_med3_f32 v69, v69, s8, v199
	v_med3_f32 v70, v70, s8, v199
	v_med3_f32 v71, v71, s8, v199
	v_pk_add_f32 v[160:161], v[160:161], 1.0 op_sel_hi:[1,0]
	v_pk_add_f32 v[162:163], v[162:163], 1.0 op_sel_hi:[1,0]
	v_pk_fma_f32 v[68:69], v[68:69], s[100:101], s[100:101]
	v_pk_fma_f32 v[70:71], v[70:71], s[100:101], s[100:101]
	v_rcp_f32_e32 v160, v160
	v_rcp_f32_e32 v161, v161
	v_rcp_f32_e32 v162, v162
	v_rcp_f32_e32 v163, v163
	v_nop
	v_pk_mul_f32 v[64:65], v[64:65], v[160:161]
	v_pk_mul_f32 v[66:67], v[66:67], v[162:163]
	v_pk_mul_f32 v[64:65], v[68:69], v[64:65]
	v_pk_mul_f32 v[66:67], v[70:71], v[66:67]
	v_cvt_pk_fp8_f32 v64, v64, v65
	v_cvt_pk_fp8_f32 v64, v66, v67 op_sel:[0,0,1]
	v_cvt_f32_i32_e32 v44, v44
	v_cvt_f32_i32_e32 v45, v45
	v_cvt_f32_i32_e32 v46, v46
	v_cvt_f32_i32_e32 v47, v47
	v_cvt_f32_i32_e32 v48, v48
	v_cvt_f32_i32_e32 v49, v49
	v_cvt_f32_i32_e32 v50, v50
	v_cvt_f32_i32_e32 v51, v51
	v_pk_mul_f32 v[202:203], v[144:145], v[156:157] op_sel:[0,1] op_sel_hi:[1,1]
	v_pk_mul_f32 v[204:205], v[146:147], v[156:157] op_sel:[0,1] op_sel_hi:[1,1]
	v_pk_fma_f32 v[44:45], v[44:45], v[202:203], v[136:137]
	v_pk_fma_f32 v[46:47], v[46:47], v[204:205], v[138:139]
; #define PG8_LAS __attribute__((address_space(3)))
;     __device__ __forceinline__ void operator()(const i32x4 (&acc)[2][2][4][2], const Unit& u, int wr, int wc, int fr, int fq, PG8_LAS unsigned* scr) const {
;     ...
;         f32x4 bgv[2], buv[2], csg[2], csu[2];
;         constexpr float C2 = 1.702f * 1.44269504f;
; #pragma unroll
;         for (int n = 0; n < 2; ++n) { bgv[n] = *(const PG8_LAS f32x4*)(scr + 512 + cl + 4 * n) * C2; buv[n] = *(const PG8_LAS f32x4*)(scr + 512 + 128 + cl + 4 * n);
;             csg[n] = *(const PG8_LAS f32x4*)(scr + 256 + cl + 4 * n) * (C2 / 127.0f); csu[n] = *(const PG8_LAS f32x4*)(scr + 256 + 128 + cl + 4 * n) * (1.0f / 127.0f); }
; #pragma unroll
;         for (int ai = 0; ai < 2; ++ai)
; #pragma unroll
;             for (int mp = 0; mp < 4; mp += 2) { unsigned wp[2][2];
; #pragma unroll
;                 for (int hm = 0; hm < 2; ++hm) { const int m = mp + hm; const int r = ai * HALF + wr * 64 + m * 16 + fr; const float rs = __uint_as_float(scr[r]); float o[8];
; #pragma unroll
;                     for (int n = 0; n < 2; ++n) { const f32x4 sgr = csg[n] * rs, sur = csu[n] * rs;
; #pragma unroll
;                         for (int q = 0; q < 4; ++q) { const float h = fminf(__builtin_fmaf((float)acc[ai][0][m][n][q], sgr[q], bgv[n][q]), 7.0f * C2), up = fminf(fmaxf(__builtin_fmaf((float)acc[ai][1][m][n][q], sur[q], buv[n][q]), -7.0f), 7.0f);
;                             const float sg = __builtin_amdgcn_rcpf(1.0f + __builtin_amdgcn_exp2f(-h)); o[4 * n + q] = __builtin_fmaf(up, ACT_SC / C2, ACT_SC / C2) * (h * sg); } }
;                     int w0 = __builtin_amdgcn_cvt_pk_fp8_f32(o[0], o[1], 0, false); w0 = __builtin_amdgcn_cvt_pk_fp8_f32(o[2], o[3], w0, true);
;                     int w1 = __builtin_amdgcn_cvt_pk_fp8_f32(o[4], o[5], 0, false); w1 = __builtin_amdgcn_cvt_pk_fp8_f32(o[6], o[7], w1, true);
;                     wp[hm][0] = (unsigned)w0; wp[hm][1] = (unsigned)w1; }
	v_pk_mul_f32 v[202:203], v[148:149], v[156:157] op_sel:[0,1] op_sel_hi:[1,1]
	v_pk_mul_f32 v[204:205], v[150:151], v[156:157] op_sel:[0,1] op_sel_hi:[1,1]
	v_min_f32_e32 v44, 0x41898193, v44
	v_min_f32_e32 v45, 0x41898193, v45
	v_min_f32_e32 v46, 0x41898193, v46
	v_min_f32_e32 v47, 0x41898193, v47
	v_pk_fma_f32 v[48:49], v[48:49], v[202:203], v[140:141]
	v_pk_fma_f32 v[50:51], v[50:51], v[204:205], v[142:143]
	v_exp_f32_e64 v202, -v44
	v_exp_f32_e64 v203, -v45
	v_exp_f32_e64 v204, -v46
	v_exp_f32_e64 v205, -v47
	v_med3_f32 v48, v48, s8, v199
	v_med3_f32 v49, v49, s8, v199
	v_med3_f32 v50, v50, s8, v199
	v_med3_f32 v51, v51, s8, v199
	v_pk_add_f32 v[202:203], v[202:203], 1.0 op_sel_hi:[1,0]
	v_pk_add_f32 v[204:205], v[204:205], 1.0 op_sel_hi:[1,0]
	v_pk_fma_f32 v[48:49], v[48:49], s[100:101], s[100:101]
	v_pk_fma_f32 v[50:51], v[50:51], s[100:101], s[100:101]
	v_rcp_f32_e32 v202, v202
	v_rcp_f32_e32 v203, v203
	v_rcp_f32_e32 v204, v204
	v_rcp_f32_e32 v205, v205
	v_nop
	v_pk_mul_f32 v[44:45], v[44:45], v[202:203]
	v_pk_mul_f32 v[46:47], v[46:47], v[204:205]
	v_pk_mul_f32 v[44:45], v[48:49], v[44:45]
	v_pk_mul_f32 v[46:47], v[50:51], v[46:47]
	v_cvt_pk_fp8_f32 v66, v44, v45
	v_cvt_pk_fp8_f32 v66, v46, v47 op_sel:[0,0,1]
	v_cvt_f32_i32_e32 v24, v24
	v_cvt_f32_i32_e32 v25, v25
	v_cvt_f32_i32_e32 v26, v26
	v_cvt_f32_i32_e32 v27, v27
	v_cvt_f32_i32_e32 v28, v28
	v_cvt_f32_i32_e32 v29, v29
	v_cvt_f32_i32_e32 v30, v30
	v_cvt_f32_i32_e32 v31, v31
	v_pk_mul_f32 v[160:161], v[144:145], v[158:159] op_sel_hi:[1,0]
	v_pk_mul_f32 v[162:163], v[146:147], v[158:159] op_sel_hi:[1,0]
	v_pk_fma_f32 v[24:25], v[24:25], v[160:161], v[136:137]
	v_pk_fma_f32 v[26:27], v[26:27], v[162:163], v[138:139]
	v_pk_mul_f32 v[160:161], v[148:149], v[158:159] op_sel_hi:[1,0]
	v_pk_mul_f32 v[162:163], v[150:151], v[158:159] op_sel_hi:[1,0]
	v_min_f32_e32 v24, 0x41898193, v24
	v_min_f32_e32 v25, 0x41898193, v25
	v_min_f32_e32 v26, 0x41898193, v26
	v_min_f32_e32 v27, 0x41898193, v27
	v_pk_fma_f32 v[28:29], v[28:29], v[160:161], v[140:141]
	v_pk_fma_f32 v[30:31], v[30:31], v[162:163], v[142:143]
	v_exp_f32_e64 v160, -v24
	v_exp_f32_e64 v161, -v25
	v_exp_f32_e64 v162, -v26
	v_exp_f32_e64 v163, -v27
	v_med3_f32 v28, v28, s8, v199
	v_med3_f32 v29, v29, s8, v199
	v_med3_f32 v30, v30, s8, v199
	v_med3_f32 v31, v31, s8, v199
	v_pk_add_f32 v[160:161], v[160:161], 1.0 op_sel_hi:[1,0]
	v_pk_add_f32 v[162:163], v[162:163], 1.0 op_sel_hi:[1,0]
	v_pk_fma_f32 v[28:29], v[28:29], s[100:101], s[100:101]
	v_pk_fma_f32 v[30:31], v[30:31], s[100:101], s[100:101]
	v_rcp_f32_e32 v160, v160
	v_rcp_f32_e32 v161, v161
	v_rcp_f32_e32 v162, v162
	v_rcp_f32_e32 v163, v163
	v_nop
	v_pk_mul_f32 v[24:25], v[24:25], v[160:161]
	v_pk_mul_f32 v[26:27], v[26:27], v[162:163]
	v_pk_mul_f32 v[24:25], v[28:29], v[24:25]
	v_pk_mul_f32 v[26:27], v[30:31], v[26:27]
	v_cvt_pk_fp8_f32 v24, v24, v25
	v_cvt_pk_fp8_f32 v24, v26, v27 op_sel:[0,0,1]
	v_cvt_f32_i32_e32 v8, v8
	v_cvt_f32_i32_e32 v9, v9
	v_cvt_f32_i32_e32 v10, v10
	v_cvt_f32_i32_e32 v11, v11
	v_cvt_f32_i32_e32 v12, v12
	v_cvt_f32_i32_e32 v13, v13
	v_cvt_f32_i32_e32 v14, v14
	v_cvt_f32_i32_e32 v15, v15
	v_pk_mul_f32 v[202:203], v[144:145], v[158:159] op_sel:[0,1] op_sel_hi:[1,1]
	v_pk_mul_f32 v[204:205], v[146:147], v[158:159] op_sel:[0,1] op_sel_hi:[1,1]
	v_pk_fma_f32 v[8:9], v[8:9], v[202:203], v[136:137]
	v_pk_fma_f32 v[10:11], v[10:11], v[204:205], v[138:139]
	v_pk_mul_f32 v[202:203], v[148:149], v[158:159] op_sel:[0,1] op_sel_hi:[1,1]
	v_pk_mul_f32 v[204:205], v[150:151], v[158:159] op_sel:[0,1] op_sel_hi:[1,1]
	v_min_f32_e32 v8, 0x41898193, v8
	v_min_f32_e32 v9, 0x41898193, v9
	v_min_f32_e32 v10, 0x41898193, v10
	v_min_f32_e32 v11, 0x41898193, v11
	v_pk_fma_f32 v[12:13], v[12:13], v[202:203], v[140:141]
	v_pk_fma_f32 v[14:15], v[14:15], v[204:205], v[142:143]
	v_exp_f32_e64 v202, -v8
	v_exp_f32_e64 v203, -v9
	v_exp_f32_e64 v204, -v10
	v_exp_f32_e64 v205, -v11
	v_med3_f32 v12, v12, s8, v199
	v_med3_f32 v13, v13, s8, v199
	v_med3_f32 v14, v14, s8, v199
	v_med3_f32 v15, v15, s8, v199
	v_pk_add_f32 v[202:203], v[202:203], 1.0 op_sel_hi:[1,0]
	v_pk_add_f32 v[204:205], v[204:205], 1.0 op_sel_hi:[1,0]
	v_pk_fma_f32 v[12:13], v[12:13], s[100:101], s[100:101]
	v_pk_fma_f32 v[14:15], v[14:15], s[100:101], s[100:101]
	v_rcp_f32_e32 v202, v202
	v_rcp_f32_e32 v203, v203
	v_rcp_f32_e32 v204, v204
	v_rcp_f32_e32 v205, v205
	v_nop
	v_pk_mul_f32 v[8:9], v[8:9], v[202:203]
	v_pk_mul_f32 v[10:11], v[10:11], v[204:205]
	v_pk_mul_f32 v[8:9], v[12:13], v[8:9]
	v_pk_mul_f32 v[10:11], v[14:15], v[10:11]
	v_cvt_pk_fp8_f32 v26, v8, v9
	v_cvt_pk_fp8_f32 v26, v10, v11 op_sel:[0,0,1]
	v_add_u32_e32 v160, 0x21110, v208
	ds_read_b128 v[136:139], v160
	v_add_u32_e32 v160, 0x21310, v208
	ds_read_b128 v[140:143], v160
	v_add_u32_e32 v160, 0x20d10, v208
	ds_read_b128 v[144:147], v160
	v_add_u32_e32 v160, 0x20f10, v208
	ds_read_b128 v[148:151], v160
	s_waitcnt lgkmcnt(0)
; #define GAS __attribute__((address_space(1)))
;     __device__ __forceinline__ void operator()(const i32x4 (&acc)[2][2][4][2], const Unit& u, int wr, int wc, int fr, int fq, PG8_LAS unsigned* scr) const {
;     ...
;                 for (int hm = 0; hm < 2; ++hm) { const int m = mp + hm; const int r = ai * HALF + wr * 64 + m * 16 + fr; const float rs = __uint_as_float(scr[r]); float o[8];
; #pragma unroll
;                     for (int n = 0; n < 2; ++n) { const f32x4 sgr = csg[n] * rs, sur = csu[n] * rs;
; #pragma unroll
;                         for (int q = 0; q < 4; ++q) { const float h = fminf(__builtin_fmaf((float)acc[ai][0][m][n][q], sgr[q], bgv[n][q]), 7.0f * C2), up = fminf(fmaxf(__builtin_fmaf((float)acc[ai][1][m][n][q], sur[q], buv[n][q]), -7.0f), 7.0f);
;                             const float sg = __builtin_amdgcn_rcpf(1.0f + __builtin_amdgcn_exp2f(-h)); o[4 * n + q] = __builtin_fmaf(up, ACT_SC / C2, ACT_SC / C2) * (h * sg); } }
;                     int w0 = __builtin_amdgcn_cvt_pk_fp8_f32(o[0], o[1], 0, false); w0 = __builtin_amdgcn_cvt_pk_fp8_f32(o[2], o[3], w0, true);
;                     int w1 = __builtin_amdgcn_cvt_pk_fp8_f32(o[4], o[5], 0, false); w1 = __builtin_amdgcn_cvt_pk_fp8_f32(o[6], o[7], w1, true);
;                     wp[hm][0] = (unsigned)w0; wp[hm][1] = (unsigned)w1; }
;                 { auto r0 = __builtin_amdgcn_permlane16_swap(wp[0][0], wp[1][0], false, false); wp[0][0] = r0[0]; wp[1][0] = r0[1];
;                   auto r1 = __builtin_amdgcn_permlane16_swap(wp[0][1], wp[1][1], false, false); wp[0][1] = r1[0]; wp[1][1] = r1[1]; }
;                 const int odd = fq & 1;
;                 const size_t arow = (size_t)(row0 + ai * HALF + (mp + odd) * 16);
;                 *(GAS u32x4*)(act + arow * 1024 + (c0 - 8 * odd)) = (u32x4){wp[0][0], wp[0][1], wp[1][0], wp[1][1]};
	v_mul_f32_e32 v136, 0x401d265f, v136
	v_mul_f32_e32 v137, 0x401d265f, v137
	v_mul_f32_e32 v138, 0x401d265f, v138
	v_mul_f32_e32 v139, 0x401d265f, v139
	v_mul_f32_e32 v144, 0x3c9e6325, v144
	v_mul_f32_e32 v145, 0x3c9e6325, v145
	v_mul_f32_e32 v146, 0x3c9e6325, v146
	v_mul_f32_e32 v147, 0x3c9e6325, v147
	v_mul_f32_e32 v148, 0x3c010204, v148
	v_mul_f32_e32 v149, 0x3c010204, v149
	v_mul_f32_e32 v150, 0x3c010204, v150
	v_mul_f32_e32 v151, 0x3c010204, v151
	v_cvt_f32_i32_e32 v120, v120
	v_cvt_f32_i32_e32 v121, v121
	v_cvt_f32_i32_e32 v122, v122
	v_cvt_f32_i32_e32 v123, v123
	v_cvt_f32_i32_e32 v124, v124
	v_cvt_f32_i32_e32 v125, v125
	v_cvt_f32_i32_e32 v126, v126
	v_cvt_f32_i32_e32 v127, v127
	v_pk_mul_f32 v[160:161], v[144:145], v[152:153] op_sel_hi:[1,0]
	v_pk_mul_f32 v[162:163], v[146:147], v[152:153] op_sel_hi:[1,0]
	v_pk_fma_f32 v[120:121], v[120:121], v[160:161], v[136:137]
	v_pk_fma_f32 v[122:123], v[122:123], v[162:163], v[138:139]
	v_pk_mul_f32 v[160:161], v[148:149], v[152:153] op_sel_hi:[1,0]
	v_pk_mul_f32 v[162:163], v[150:151], v[152:153] op_sel_hi:[1,0]
	v_min_f32_e32 v120, 0x41898193, v120
	v_min_f32_e32 v121, 0x41898193, v121
	v_min_f32_e32 v122, 0x41898193, v122
	v_min_f32_e32 v123, 0x41898193, v123
	v_pk_fma_f32 v[124:125], v[124:125], v[160:161], v[140:141]
	v_pk_fma_f32 v[126:127], v[126:127], v[162:163], v[142:143]
	v_exp_f32_e64 v160, -v120
	v_exp_f32_e64 v161, -v121
	v_exp_f32_e64 v162, -v122
	v_exp_f32_e64 v163, -v123
	v_med3_f32 v124, v124, s8, v199
	v_med3_f32 v125, v125, s8, v199
	v_med3_f32 v126, v126, s8, v199
	v_med3_f32 v127, v127, s8, v199
	v_pk_add_f32 v[160:161], v[160:161], 1.0 op_sel_hi:[1,0]
	v_pk_add_f32 v[162:163], v[162:163], 1.0 op_sel_hi:[1,0]
	v_pk_fma_f32 v[124:125], v[124:125], s[100:101], s[100:101]
	v_pk_fma_f32 v[126:127], v[126:127], s[100:101], s[100:101]
	v_rcp_f32_e32 v160, v160
	v_rcp_f32_e32 v161, v161
	v_rcp_f32_e32 v162, v162
	v_rcp_f32_e32 v163, v163
	v_nop
	v_pk_mul_f32 v[120:121], v[120:121], v[160:161]
	v_pk_mul_f32 v[122:123], v[122:123], v[162:163]
	v_pk_mul_f32 v[120:121], v[124:125], v[120:121]
	v_pk_mul_f32 v[122:123], v[126:127], v[122:123]
	v_cvt_pk_fp8_f32 v129, v120, v121
	v_cvt_pk_fp8_f32 v129, v122, v123 op_sel:[0,0,1]
	v_cvt_f32_i32_e32 v104, v104
	v_cvt_f32_i32_e32 v105, v105
	v_cvt_f32_i32_e32 v106, v106
	v_cvt_f32_i32_e32 v107, v107
	v_cvt_f32_i32_e32 v108, v108
	v_cvt_f32_i32_e32 v109, v109
	v_cvt_f32_i32_e32 v110, v110
	v_cvt_f32_i32_e32 v111, v111
	v_pk_mul_f32 v[202:203], v[144:145], v[152:153] op_sel:[0,1] op_sel_hi:[1,1]
	v_pk_mul_f32 v[204:205], v[146:147], v[152:153] op_sel:[0,1] op_sel_hi:[1,1]
	v_pk_fma_f32 v[104:105], v[104:105], v[202:203], v[136:137]
	v_pk_fma_f32 v[106:107], v[106:107], v[204:205], v[138:139]
	v_pk_mul_f32 v[202:203], v[148:149], v[152:153] op_sel:[0,1] op_sel_hi:[1,1]
	v_pk_mul_f32 v[204:205], v[150:151], v[152:153] op_sel:[0,1] op_sel_hi:[1,1]
	v_min_f32_e32 v104, 0x41898193, v104
	v_min_f32_e32 v105, 0x41898193, v105
	v_min_f32_e32 v106, 0x41898193, v106
	v_min_f32_e32 v107, 0x41898193, v107
	v_pk_fma_f32 v[108:109], v[108:109], v[202:203], v[140:141]
	v_pk_fma_f32 v[110:111], v[110:111], v[204:205], v[142:143]
	v_exp_f32_e64 v202, -v104
	v_exp_f32_e64 v203, -v105
	v_exp_f32_e64 v204, -v106
	v_exp_f32_e64 v205, -v107
	v_med3_f32 v108, v108, s8, v199
	v_med3_f32 v109, v109, s8, v199
	v_med3_f32 v110, v110, s8, v199
	v_med3_f32 v111, v111, s8, v199
	v_pk_add_f32 v[202:203], v[202:203], 1.0 op_sel_hi:[1,0]
	v_pk_add_f32 v[204:205], v[204:205], 1.0 op_sel_hi:[1,0]
	v_pk_fma_f32 v[108:109], v[108:109], s[100:101], s[100:101]
	v_pk_fma_f32 v[110:111], v[110:111], s[100:101], s[100:101]
	v_rcp_f32_e32 v202, v202
	v_rcp_f32_e32 v203, v203
	v_rcp_f32_e32 v204, v204
	v_rcp_f32_e32 v205, v205
	v_nop
	v_pk_mul_f32 v[104:105], v[104:105], v[202:203]
	v_pk_mul_f32 v[106:107], v[106:107], v[204:205]
	v_pk_mul_f32 v[104:105], v[108:109], v[104:105]
	v_pk_mul_f32 v[106:107], v[110:111], v[106:107]
	v_cvt_pk_fp8_f32 v131, v104, v105
	v_cvt_pk_fp8_f32 v131, v106, v107 op_sel:[0,0,1]
	s_nop 1
	v_permlane16_swap_b32_e32 v128, v130
	v_permlane16_swap_b32_e32 v129, v131
	v_add_u32_e32 v160, 0, v185
	v_mov_b32_e32 v161, 0
	v_lshlrev_b64 v[160:161], 10, v[160:161]
	v_lshl_add_u64 v[160:161], s[60:61], 0, v[160:161]
	v_lshl_add_u64 v[160:161], v[160:161], 0, v[206:207]
	global_store_dwordx4 v[160:161], v[128:131], off
	v_cvt_f32_i32_e32 v88, v88
	v_cvt_f32_i32_e32 v89, v89
	v_cvt_f32_i32_e32 v90, v90
	v_cvt_f32_i32_e32 v91, v91
	v_cvt_f32_i32_e32 v92, v92
	v_cvt_f32_i32_e32 v93, v93
	v_cvt_f32_i32_e32 v94, v94
	v_cvt_f32_i32_e32 v95, v95
	v_pk_mul_f32 v[160:161], v[144:145], v[154:155] op_sel_hi:[1,0]
	v_pk_mul_f32 v[162:163], v[146:147], v[154:155] op_sel_hi:[1,0]
	v_pk_fma_f32 v[88:89], v[88:89], v[160:161], v[136:137]
	v_pk_fma_f32 v[90:91], v[90:91], v[162:163], v[138:139]
	v_pk_mul_f32 v[160:161], v[148:149], v[154:155] op_sel_hi:[1,0]
	v_pk_mul_f32 v[162:163], v[150:151], v[154:155] op_sel_hi:[1,0]
	v_min_f32_e32 v88, 0x41898193, v88
	v_min_f32_e32 v89, 0x41898193, v89
	v_min_f32_e32 v90, 0x41898193, v90
	v_min_f32_e32 v91, 0x41898193, v91
	v_pk_fma_f32 v[92:93], v[92:93], v[160:161], v[140:141]
	v_pk_fma_f32 v[94:95], v[94:95], v[162:163], v[142:143]
	v_exp_f32_e64 v160, -v88
	v_exp_f32_e64 v161, -v89
	v_exp_f32_e64 v162, -v90
	v_exp_f32_e64 v163, -v91
	v_med3_f32 v92, v92, s8, v199
	v_med3_f32 v93, v93, s8, v199
	v_med3_f32 v94, v94, s8, v199
	v_med3_f32 v95, v95, s8, v199
	v_pk_add_f32 v[160:161], v[160:161], 1.0 op_sel_hi:[1,0]
	v_pk_add_f32 v[162:163], v[162:163], 1.0 op_sel_hi:[1,0]
	v_pk_fma_f32 v[92:93], v[92:93], s[100:101], s[100:101]
; #define GAS __attribute__((address_space(1)))
;     __device__ __forceinline__ void operator()(const i32x4 (&acc)[2][2][4][2], const Unit& u, int wr, int wc, int fr, int fq, PG8_LAS unsigned* scr) const {
;     ...
;                 for (int hm = 0; hm < 2; ++hm) { const int m = mp + hm; const int r = ai * HALF + wr * 64 + m * 16 + fr; const float rs = __uint_as_float(scr[r]); float o[8];
; #pragma unroll
;                     for (int n = 0; n < 2; ++n) { const f32x4 sgr = csg[n] * rs, sur = csu[n] * rs;
; #pragma unroll
;                         for (int q = 0; q < 4; ++q) { const float h = fminf(__builtin_fmaf((float)acc[ai][0][m][n][q], sgr[q], bgv[n][q]), 7.0f * C2), up = fminf(fmaxf(__builtin_fmaf((float)acc[ai][1][m][n][q], sur[q], buv[n][q]), -7.0f), 7.0f);
;                             const float sg = __builtin_amdgcn_rcpf(1.0f + __builtin_amdgcn_exp2f(-h)); o[4 * n + q] = __builtin_fmaf(up, ACT_SC / C2, ACT_SC / C2) * (h * sg); } }
;                     int w0 = __builtin_amdgcn_cvt_pk_fp8_f32(o[0], o[1], 0, false); w0 = __builtin_amdgcn_cvt_pk_fp8_f32(o[2], o[3], w0, true);
;                     int w1 = __builtin_amdgcn_cvt_pk_fp8_f32(o[4], o[5], 0, false); w1 = __builtin_amdgcn_cvt_pk_fp8_f32(o[6], o[7], w1, true);
;                     wp[hm][0] = (unsigned)w0; wp[hm][1] = (unsigned)w1; }
;                 { auto r0 = __builtin_amdgcn_permlane16_swap(wp[0][0], wp[1][0], false, false); wp[0][0] = r0[0]; wp[1][0] = r0[1];
;                   auto r1 = __builtin_amdgcn_permlane16_swap(wp[0][1], wp[1][1], false, false); wp[0][1] = r1[0]; wp[1][1] = r1[1]; }
;                 const int odd = fq & 1;
;                 const size_t arow = (size_t)(row0 + ai * HALF + (mp + odd) * 16);
;                 *(GAS u32x4*)(act + arow * 1024 + (c0 - 8 * odd)) = (u32x4){wp[0][0], wp[0][1], wp[1][0], wp[1][1]};
	v_pk_fma_f32 v[94:95], v[94:95], s[100:101], s[100:101]
	v_rcp_f32_e32 v160, v160
	v_rcp_f32_e32 v161, v161
	v_rcp_f32_e32 v162, v162
	v_rcp_f32_e32 v163, v163
	v_nop
	v_pk_mul_f32 v[88:89], v[88:89], v[160:161]
	v_pk_mul_f32 v[90:91], v[90:91], v[162:163]
	v_pk_mul_f32 v[88:89], v[92:93], v[88:89]
	v_pk_mul_f32 v[90:91], v[94:95], v[90:91]
	v_cvt_pk_fp8_f32 v97, v88, v89
	v_cvt_pk_fp8_f32 v97, v90, v91 op_sel:[0,0,1]
	v_cvt_f32_i32_e32 v72, v72
	v_cvt_f32_i32_e32 v73, v73
	v_cvt_f32_i32_e32 v74, v74
	v_cvt_f32_i32_e32 v75, v75
	v_cvt_f32_i32_e32 v76, v76
	v_cvt_f32_i32_e32 v77, v77
	v_cvt_f32_i32_e32 v78, v78
	v_cvt_f32_i32_e32 v79, v79
	v_pk_mul_f32 v[202:203], v[144:145], v[154:155] op_sel:[0,1] op_sel_hi:[1,1]
	v_pk_mul_f32 v[204:205], v[146:147], v[154:155] op_sel:[0,1] op_sel_hi:[1,1]
	v_pk_fma_f32 v[72:73], v[72:73], v[202:203], v[136:137]
	v_pk_fma_f32 v[74:75], v[74:75], v[204:205], v[138:139]
	v_pk_mul_f32 v[202:203], v[148:149], v[154:155] op_sel:[0,1] op_sel_hi:[1,1]
	v_pk_mul_f32 v[204:205], v[150:151], v[154:155] op_sel:[0,1] op_sel_hi:[1,1]
	v_min_f32_e32 v72, 0x41898193, v72
	v_min_f32_e32 v73, 0x41898193, v73
	v_min_f32_e32 v74, 0x41898193, v74
	v_min_f32_e32 v75, 0x41898193, v75
	v_pk_fma_f32 v[76:77], v[76:77], v[202:203], v[140:141]
	v_pk_fma_f32 v[78:79], v[78:79], v[204:205], v[142:143]
	v_exp_f32_e64 v202, -v72
	v_exp_f32_e64 v203, -v73
	v_exp_f32_e64 v204, -v74
	v_exp_f32_e64 v205, -v75
	v_med3_f32 v76, v76, s8, v199
	v_med3_f32 v77, v77, s8, v199
	v_med3_f32 v78, v78, s8, v199
	v_med3_f32 v79, v79, s8, v199
	v_pk_add_f32 v[202:203], v[202:203], 1.0 op_sel_hi:[1,0]
	v_pk_add_f32 v[204:205], v[204:205], 1.0 op_sel_hi:[1,0]
	v_pk_fma_f32 v[76:77], v[76:77], s[100:101], s[100:101]
	v_pk_fma_f32 v[78:79], v[78:79], s[100:101], s[100:101]
	v_rcp_f32_e32 v202, v202
	v_rcp_f32_e32 v203, v203
	v_rcp_f32_e32 v204, v204
	v_rcp_f32_e32 v205, v205
	v_nop
	v_pk_mul_f32 v[72:73], v[72:73], v[202:203]
	v_pk_mul_f32 v[74:75], v[74:75], v[204:205]
	v_pk_mul_f32 v[72:73], v[76:77], v[72:73]
	v_pk_mul_f32 v[74:75], v[78:79], v[74:75]
	v_cvt_pk_fp8_f32 v99, v72, v73
	v_cvt_pk_fp8_f32 v99, v74, v75 op_sel:[0,0,1]
	s_nop 1
	v_permlane16_swap_b32_e32 v96, v98
	v_permlane16_swap_b32_e32 v97, v99
	v_add_u32_e32 v160, 32, v185
	v_mov_b32_e32 v161, 0
	v_lshlrev_b64 v[160:161], 10, v[160:161]
	v_lshl_add_u64 v[160:161], s[60:61], 0, v[160:161]
	v_lshl_add_u64 v[160:161], v[160:161], 0, v[206:207]
	global_store_dwordx4 v[160:161], v[96:99], off
	v_cvt_f32_i32_e32 v56, v56
	v_cvt_f32_i32_e32 v57, v57
	v_cvt_f32_i32_e32 v58, v58
	v_cvt_f32_i32_e32 v59, v59
	v_cvt_f32_i32_e32 v60, v60
	v_cvt_f32_i32_e32 v61, v61
	v_cvt_f32_i32_e32 v62, v62
	v_cvt_f32_i32_e32 v63, v63
	v_pk_mul_f32 v[160:161], v[144:145], v[156:157] op_sel_hi:[1,0]
	v_pk_mul_f32 v[162:163], v[146:147], v[156:157] op_sel_hi:[1,0]
	v_pk_fma_f32 v[56:57], v[56:57], v[160:161], v[136:137]
	v_pk_fma_f32 v[58:59], v[58:59], v[162:163], v[138:139]
	v_pk_mul_f32 v[160:161], v[148:149], v[156:157] op_sel_hi:[1,0]
	v_pk_mul_f32 v[162:163], v[150:151], v[156:157] op_sel_hi:[1,0]
	v_min_f32_e32 v56, 0x41898193, v56
	v_min_f32_e32 v57, 0x41898193, v57
	v_min_f32_e32 v58, 0x41898193, v58
	v_min_f32_e32 v59, 0x41898193, v59
	v_pk_fma_f32 v[60:61], v[60:61], v[160:161], v[140:141]
	v_pk_fma_f32 v[62:63], v[62:63], v[162:163], v[142:143]
	v_exp_f32_e64 v160, -v56
	v_exp_f32_e64 v161, -v57
	v_exp_f32_e64 v162, -v58
	v_exp_f32_e64 v163, -v59
	v_med3_f32 v60, v60, s8, v199
	v_med3_f32 v61, v61, s8, v199
	v_med3_f32 v62, v62, s8, v199
	v_med3_f32 v63, v63, s8, v199
	v_pk_add_f32 v[160:161], v[160:161], 1.0 op_sel_hi:[1,0]
	v_pk_add_f32 v[162:163], v[162:163], 1.0 op_sel_hi:[1,0]
	v_pk_fma_f32 v[60:61], v[60:61], s[100:101], s[100:101]
	v_pk_fma_f32 v[62:63], v[62:63], s[100:101], s[100:101]
	v_rcp_f32_e32 v160, v160
	v_rcp_f32_e32 v161, v161
	v_rcp_f32_e32 v162, v162
	v_rcp_f32_e32 v163, v163
	v_nop
	v_pk_mul_f32 v[56:57], v[56:57], v[160:161]
	v_pk_mul_f32 v[58:59], v[58:59], v[162:163]
	v_pk_mul_f32 v[56:57], v[60:61], v[56:57]
	v_pk_mul_f32 v[58:59], v[62:63], v[58:59]
	v_cvt_pk_fp8_f32 v65, v56, v57
	v_cvt_pk_fp8_f32 v65, v58, v59 op_sel:[0,0,1]
	v_cvt_f32_i32_e32 v32, v32
	v_cvt_f32_i32_e32 v33, v33
	v_cvt_f32_i32_e32 v34, v34
	v_cvt_f32_i32_e32 v35, v35
	v_cvt_f32_i32_e32 v36, v36
	v_cvt_f32_i32_e32 v37, v37
	v_cvt_f32_i32_e32 v38, v38
	v_cvt_f32_i32_e32 v39, v39
	v_pk_mul_f32 v[202:203], v[144:145], v[156:157] op_sel:[0,1] op_sel_hi:[1,1]
	v_pk_mul_f32 v[204:205], v[146:147], v[156:157] op_sel:[0,1] op_sel_hi:[1,1]
	v_pk_fma_f32 v[32:33], v[32:33], v[202:203], v[136:137]
	v_pk_fma_f32 v[34:35], v[34:35], v[204:205], v[138:139]
	v_pk_mul_f32 v[202:203], v[148:149], v[156:157] op_sel:[0,1] op_sel_hi:[1,1]
	v_pk_mul_f32 v[204:205], v[150:151], v[156:157] op_sel:[0,1] op_sel_hi:[1,1]
	v_min_f32_e32 v32, 0x41898193, v32
	v_min_f32_e32 v33, 0x41898193, v33
	v_min_f32_e32 v34, 0x41898193, v34
	v_min_f32_e32 v35, 0x41898193, v35
	v_pk_fma_f32 v[36:37], v[36:37], v[202:203], v[140:141]
	v_pk_fma_f32 v[38:39], v[38:39], v[204:205], v[142:143]
	v_exp_f32_e64 v202, -v32
	v_exp_f32_e64 v203, -v33
	v_exp_f32_e64 v204, -v34
	v_exp_f32_e64 v205, -v35
	v_med3_f32 v36, v36, s8, v199
	v_med3_f32 v37, v37, s8, v199
	v_med3_f32 v38, v38, s8, v199
	v_med3_f32 v39, v39, s8, v199
	v_pk_add_f32 v[202:203], v[202:203], 1.0 op_sel_hi:[1,0]
	v_pk_add_f32 v[204:205], v[204:205], 1.0 op_sel_hi:[1,0]
	v_pk_fma_f32 v[36:37], v[36:37], s[100:101], s[100:101]
	v_pk_fma_f32 v[38:39], v[38:39], s[100:101], s[100:101]
	v_rcp_f32_e32 v202, v202
	v_rcp_f32_e32 v203, v203
	v_rcp_f32_e32 v204, v204
	v_rcp_f32_e32 v205, v205
	v_nop
; #define GAS __attribute__((address_space(1)))
; #define PG8_BAR __builtin_amdgcn_s_barrier()
;     __device__ __forceinline__ void operator()(const i32x4 (&acc)[2][2][4][2], const Unit& u, int wr, int wc, int fr, int fq, PG8_LAS unsigned* scr) const {
;     ...
;                 { auto r0 = __builtin_amdgcn_permlane16_swap(wp[0][0], wp[1][0], false, false); wp[0][0] = r0[0]; wp[1][0] = r0[1];
;                   auto r1 = __builtin_amdgcn_permlane16_swap(wp[0][1], wp[1][1], false, false); wp[0][1] = r1[0]; wp[1][1] = r1[1]; }
;                 const int odd = fq & 1;
;                 const size_t arow = (size_t)(row0 + ai * HALF + (mp + odd) * 16);
;                 *(GAS u32x4*)(act + arow * 1024 + (c0 - 8 * odd)) = (u32x4){wp[0][0], wp[0][1], wp[1][0], wp[1][1]};
;                 __builtin_amdgcn_sched_barrier(0); }
; template <class Epi, class Sched, bool GATHER, int MODE>
; __device__ __forceinline__ void gemm_phase(PG8_LAS unsigned char* lds, PG8_LAS unsigned* scr, const Gemm g, const Sched& S, const Epi& E, int tid_in) {
;     ...
;         if (!has_next) break;
;         cur = nxt; cA = nA; cB = nB; ++ui;
;         if (GATHER) { const u32x4 nx = gather_read(cur); c0[0] = nx[0]; c0[1] = nx[1]; c1[0] = nx[2]; c1[1] = nx[3]; }
;         if (wr == 1) PG8_BAR;
	v_pk_mul_f32 v[32:33], v[32:33], v[202:203]
	v_pk_mul_f32 v[34:35], v[34:35], v[204:205]
	v_pk_mul_f32 v[32:33], v[36:37], v[32:33]
	v_pk_mul_f32 v[34:35], v[38:39], v[34:35]
	v_cvt_pk_fp8_f32 v67, v32, v33
	v_cvt_pk_fp8_f32 v67, v34, v35 op_sel:[0,0,1]
	s_nop 1
	v_permlane16_swap_b32_e32 v64, v66
	v_permlane16_swap_b32_e32 v65, v67
	v_add_u32_e32 v160, 128, v185
	v_mov_b32_e32 v161, 0
	v_lshlrev_b64 v[160:161], 10, v[160:161]
	v_lshl_add_u64 v[160:161], s[60:61], 0, v[160:161]
	v_lshl_add_u64 v[160:161], v[160:161], 0, v[206:207]
	global_store_dwordx4 v[160:161], v[64:67], off
	v_cvt_f32_i32_e32 v16, v16
	v_cvt_f32_i32_e32 v17, v17
	v_cvt_f32_i32_e32 v18, v18
	v_cvt_f32_i32_e32 v19, v19
	v_cvt_f32_i32_e32 v20, v20
	v_cvt_f32_i32_e32 v21, v21
	v_cvt_f32_i32_e32 v22, v22
	v_cvt_f32_i32_e32 v23, v23
	v_pk_mul_f32 v[160:161], v[144:145], v[158:159] op_sel_hi:[1,0]
	v_pk_mul_f32 v[162:163], v[146:147], v[158:159] op_sel_hi:[1,0]
	v_pk_fma_f32 v[16:17], v[16:17], v[160:161], v[136:137]
	v_pk_fma_f32 v[18:19], v[18:19], v[162:163], v[138:139]
	v_pk_mul_f32 v[160:161], v[148:149], v[158:159] op_sel_hi:[1,0]
	v_pk_mul_f32 v[162:163], v[150:151], v[158:159] op_sel_hi:[1,0]
	v_min_f32_e32 v16, 0x41898193, v16
	v_min_f32_e32 v17, 0x41898193, v17
	v_min_f32_e32 v18, 0x41898193, v18
	v_min_f32_e32 v19, 0x41898193, v19
	v_pk_fma_f32 v[20:21], v[20:21], v[160:161], v[140:141]
	v_pk_fma_f32 v[22:23], v[22:23], v[162:163], v[142:143]
	v_exp_f32_e64 v160, -v16
	v_exp_f32_e64 v161, -v17
	v_exp_f32_e64 v162, -v18
	v_exp_f32_e64 v163, -v19
	v_med3_f32 v20, v20, s8, v199
	v_med3_f32 v21, v21, s8, v199
	v_med3_f32 v22, v22, s8, v199
	v_med3_f32 v23, v23, s8, v199
	v_pk_add_f32 v[160:161], v[160:161], 1.0 op_sel_hi:[1,0]
	v_pk_add_f32 v[162:163], v[162:163], 1.0 op_sel_hi:[1,0]
	v_pk_fma_f32 v[20:21], v[20:21], s[100:101], s[100:101]
	v_pk_fma_f32 v[22:23], v[22:23], s[100:101], s[100:101]
	v_rcp_f32_e32 v160, v160
	v_rcp_f32_e32 v161, v161
	v_rcp_f32_e32 v162, v162
	v_rcp_f32_e32 v163, v163
	v_nop
	v_pk_mul_f32 v[16:17], v[16:17], v[160:161]
	v_pk_mul_f32 v[18:19], v[18:19], v[162:163]
	v_pk_mul_f32 v[16:17], v[20:21], v[16:17]
	v_pk_mul_f32 v[18:19], v[22:23], v[18:19]
	v_cvt_pk_fp8_f32 v25, v16, v17
	v_cvt_pk_fp8_f32 v25, v18, v19 op_sel:[0,0,1]
	v_cvt_f32_i32_e32 v0, v0
	v_cvt_f32_i32_e32 v1, v1
	v_cvt_f32_i32_e32 v2, v2
	v_cvt_f32_i32_e32 v3, v3
	v_cvt_f32_i32_e32 v4, v4
	v_cvt_f32_i32_e32 v5, v5
	v_cvt_f32_i32_e32 v6, v6
	v_cvt_f32_i32_e32 v7, v7
	v_pk_mul_f32 v[202:203], v[144:145], v[158:159] op_sel:[0,1] op_sel_hi:[1,1]
	v_pk_mul_f32 v[204:205], v[146:147], v[158:159] op_sel:[0,1] op_sel_hi:[1,1]
	v_pk_fma_f32 v[0:1], v[0:1], v[202:203], v[136:137]
	v_pk_fma_f32 v[2:3], v[2:3], v[204:205], v[138:139]
	v_pk_mul_f32 v[202:203], v[148:149], v[158:159] op_sel:[0,1] op_sel_hi:[1,1]
	v_pk_mul_f32 v[204:205], v[150:151], v[158:159] op_sel:[0,1] op_sel_hi:[1,1]
	v_min_f32_e32 v0, 0x41898193, v0
	v_min_f32_e32 v1, 0x41898193, v1
	v_min_f32_e32 v2, 0x41898193, v2
	v_min_f32_e32 v3, 0x41898193, v3
	v_pk_fma_f32 v[4:5], v[4:5], v[202:203], v[140:141]
	v_pk_fma_f32 v[6:7], v[6:7], v[204:205], v[142:143]
	v_exp_f32_e64 v202, -v0
	v_exp_f32_e64 v203, -v1
	v_exp_f32_e64 v204, -v2
	v_exp_f32_e64 v205, -v3
	v_med3_f32 v4, v4, s8, v199
	v_med3_f32 v5, v5, s8, v199
	v_med3_f32 v6, v6, s8, v199
	v_med3_f32 v7, v7, s8, v199
	v_pk_add_f32 v[202:203], v[202:203], 1.0 op_sel_hi:[1,0]
	v_pk_add_f32 v[204:205], v[204:205], 1.0 op_sel_hi:[1,0]
	v_pk_fma_f32 v[4:5], v[4:5], s[100:101], s[100:101]
	v_pk_fma_f32 v[6:7], v[6:7], s[100:101], s[100:101]
	v_rcp_f32_e32 v202, v202
	v_rcp_f32_e32 v203, v203
	v_rcp_f32_e32 v204, v204
	v_rcp_f32_e32 v205, v205
	v_nop
	v_pk_mul_f32 v[0:1], v[0:1], v[202:203]
	v_pk_mul_f32 v[2:3], v[2:3], v[204:205]
	v_pk_mul_f32 v[0:1], v[4:5], v[0:1]
	v_pk_mul_f32 v[2:3], v[6:7], v[2:3]
	v_cvt_pk_fp8_f32 v27, v0, v1
	v_cvt_pk_fp8_f32 v27, v2, v3 op_sel:[0,0,1]
	s_nop 1
	v_permlane16_swap_b32_e32 v24, v26
	v_permlane16_swap_b32_e32 v25, v27
	v_add_u32_e32 v160, 160, v185
	v_mov_b32_e32 v161, 0
	v_lshlrev_b64 v[160:161], 10, v[160:161]
	v_lshl_add_u64 v[160:161], s[60:61], 0, v[160:161]
	v_lshl_add_u64 v[160:161], v[160:161], 0, v[206:207]
	global_store_dwordx4 v[160:161], v[24:27], off
	s_cmp_eq_u32 s38, s89
	s_mov_b64 s[10:11], -1
	s_cbranch_scc1 .LBB0_786
	v_mov_b32_e32 v0, v168
	s_andn2_b64 vcc, exec, s[58:59]
	v_ashrrev_i32_e32 v2, 31, v0
	v_lshrrev_b32_e32 v2, 26, v2
	v_lshlrev_b32_e32 v6, 4, v0
	v_lshl_add_u32 v1, v0, 2, 0
	v_add_u32_e32 v2, v0, v2
	v_bfe_i32 v0, v0, 27, 1
	v_lshrrev_b32_e32 v0, 22, v0
	v_add_u32_e32 v0, v6, v0
	v_and_b32_e32 v0, 0xfffffc00, v0
	v_sub_u32_e32 v0, v6, v0
	v_ashrrev_i32_e32 v4, 6, v2
	v_lshrrev_b32_e32 v2, 4, v0
	v_bitop3_b32 v5, v2, v0, 32 bitop3:0x6c
	v_ashrrev_i32_e32 v2, 31, v5
	v_lshrrev_b32_e32 v2, 26, v2
	v_lshlrev_b32_e32 v0, 3, v4
	v_add_u32_e32 v7, v5, v2
	v_and_b32_e32 v0, -16, v0
	v_ashrrev_i32_e32 v2, 6, v7
	v_add3_u32 v8, v0, s23, v2
	v_cmp_gt_i32_e64 s[40:41], s92, v8
	v_add_u32_e32 v8, 0x80, v8
	v_cmp_gt_i32_e64 s[38:39], s92, v8
	v_add_u32_e32 v8, 0x2000, v6
	v_ashrrev_i32_e32 v6, 31, v8
	v_lshrrev_b32_e32 v6, 22, v6
	v_add_u32_e32 v6, v8, v6
	v_ashrrev_i32_e32 v6, 10, v6
	v_mul_i32_i24_e32 v9, 0x400, v6
	v_sub_u32_e32 v8, v8, v9
	v_lshrrev_b32_e32 v9, 4, v8
	v_bitop3_b32 v8, v9, v8, 32 bitop3:0x6c
	v_lshlrev_b32_e32 v9, 3, v6
	v_and_b32_e32 v10, -16, v9
	v_ashrrev_i32_e32 v9, 31, v8
	v_add_u32_e32 v1, 0x21900, v1
	v_lshrrev_b32_e32 v9, 26, v9
	ds_read2st64_b32 v[2:3], v1 offset1:8
	ds_read2st64_b32 v[0:1], v1 offset0:16 offset1:24
	v_add_u32_e32 v9, v8, v9
	v_ashrrev_i32_e32 v11, 6, v9
	v_add3_u32 v10, v10, s23, v11
	v_cmp_gt_i32_e64 s[42:43], s92, v10
	v_add_u32_e32 v10, 0x80, v10
	v_cmp_gt_i32_e64 s[44:45], s92, v10
	s_cbranch_vccnz .LBB0_785
	s_barrier
	s_branch .LBB0_785

; __device__ __forceinline__ void p7_combine(Frame& F, int l) {
;     ...
;         for (int r = 0; r < 4; ++r) {
; #pragma unroll
;             for (int j = 0; j < 4; ++j) { const int hw = (int)hv[r][j]; f32x4 a; a.x = (float)((hw << 24) >> 24) * hsa[r]; a.y = (float)((hw << 16) >> 24) * hsa[r]; a.z = (float)((hw << 8) >> 24) * hsa[r]; a.w = (float)(hw >> 24) * hsa[r];
;                 f32x4 ys = (f32x4){0.f, 0.f, 0.f, 0.f};
; #pragma unroll
;                 for (int k = 0; k < 4; ++k) { const int w = (int)yv[r][k][j]; ys.x += __builtin_amdgcn_cvt_f32_fp8(w, 0); ys.y += __builtin_amdgcn_cvt_f32_fp8(w, 1); ys.z += __builtin_amdgcn_cvt_f32_fp8(w, 2); ys.w += __builtin_amdgcn_cvt_f32_fp8(w, 3); }
;                 v[r][j] = a + ys * (1.0f / 16.0f); }
.LBB0_1061:
	s_waitcnt vmcnt(44)
	v_mul_f32_e32 v16, 0x3fb504f3, v1
	v_cvt_f32_fp8_e32 v0, v95
	v_cvt_f32_fp8_sdwa v1, v95 src0_sel:BYTE_1
	v_cvt_f32_fp8_sdwa v4, v95 src0_sel:BYTE_2
	v_cvt_f32_fp8_sdwa v5, v95 src0_sel:BYTE_3
	v_cvt_f32_fp8_e32 v6, v96
	v_cvt_f32_fp8_sdwa v7, v96 src0_sel:BYTE_1
	v_cvt_f32_fp8_sdwa v8, v96 src0_sel:BYTE_2
	v_cvt_f32_fp8_sdwa v9, v96 src0_sel:BYTE_3
	v_cvt_f32_fp8_e32 v10, v97
	v_cvt_f32_fp8_sdwa v11, v97 src0_sel:BYTE_1
	v_cvt_f32_fp8_sdwa v12, v97 src0_sel:BYTE_2
	v_cvt_f32_fp8_sdwa v13, v97 src0_sel:BYTE_3
	v_cvt_f32_fp8_e32 v14, v98
	v_cvt_f32_fp8_sdwa v15, v98 src0_sel:BYTE_1
	v_cvt_f32_fp8_sdwa v18, v98 src0_sel:BYTE_2
	v_cvt_f32_fp8_sdwa v19, v98 src0_sel:BYTE_3
	v_pk_add_f32 v[0:1], v[0:1], 0 op_sel_hi:[1,0]
	v_pk_add_f32 v[4:5], v[4:5], 0 op_sel_hi:[1,0]
	v_pk_add_f32 v[0:1], v[0:1], v[6:7]
	v_pk_add_f32 v[4:5], v[4:5], v[8:9]
	v_cvt_f32_i32_sdwa v7, sext(v94) dst_sel:DWORD dst_unused:UNUSED_PAD src0_sel:BYTE_3
	v_cvt_f32_i32_sdwa v9, sext(v94) dst_sel:DWORD dst_unused:UNUSED_PAD src0_sel:BYTE_1
	v_cvt_f32_i32_sdwa v8, sext(v94) dst_sel:DWORD dst_unused:UNUSED_PAD src0_sel:BYTE_0
	v_cvt_f32_i32_sdwa v6, sext(v94) dst_sel:DWORD dst_unused:UNUSED_PAD src0_sel:BYTE_2
	v_pk_add_f32 v[0:1], v[0:1], v[10:11]
	v_pk_add_f32 v[4:5], v[4:5], v[12:13]
	v_pk_add_f32 v[0:1], v[0:1], v[14:15]
	v_pk_add_f32 v[4:5], v[4:5], v[18:19]
	s_mov_b32 s10, 0x3d800000
	v_pk_mul_f32 v[0:1], v[0:1], s[10:11] op_sel_hi:[1,0]
	v_pk_mul_f32 v[4:5], v[4:5], s[10:11] op_sel_hi:[1,0]
	v_cvt_f32_fp8_e32 v10, v91
	v_pk_fma_f32 v[4:5], v[16:17], v[6:7], v[4:5] op_sel_hi:[0,1,1]
	v_pk_fma_f32 v[6:7], v[16:17], v[8:9], v[0:1] op_sel_hi:[0,1,1]
	v_cvt_f32_fp8_e32 v0, v90
	v_cvt_f32_fp8_sdwa v1, v90 src0_sel:BYTE_1
	v_cvt_f32_fp8_sdwa v8, v90 src0_sel:BYTE_2
	v_cvt_f32_fp8_sdwa v9, v90 src0_sel:BYTE_3
	v_cvt_f32_fp8_sdwa v11, v91 src0_sel:BYTE_1
	v_cvt_f32_fp8_sdwa v12, v91 src0_sel:BYTE_2
	v_cvt_f32_fp8_sdwa v13, v91 src0_sel:BYTE_3
	v_cvt_f32_fp8_e32 v14, v92
	v_cvt_f32_fp8_sdwa v15, v92 src0_sel:BYTE_1
	v_cvt_f32_fp8_sdwa v18, v92 src0_sel:BYTE_2
	v_cvt_f32_fp8_sdwa v19, v92 src0_sel:BYTE_3
	v_cvt_f32_fp8_e32 v20, v93
	v_cvt_f32_fp8_sdwa v21, v93 src0_sel:BYTE_1
	v_cvt_f32_fp8_sdwa v22, v93 src0_sel:BYTE_2
	v_cvt_f32_fp8_sdwa v23, v93 src0_sel:BYTE_3
	v_pk_add_f32 v[0:1], v[0:1], 0 op_sel_hi:[1,0]
	v_pk_add_f32 v[8:9], v[8:9], 0 op_sel_hi:[1,0]
	v_pk_add_f32 v[0:1], v[0:1], v[10:11]
	v_pk_add_f32 v[8:9], v[8:9], v[12:13]
	v_cvt_f32_i32_sdwa v11, sext(v89) dst_sel:DWORD dst_unused:UNUSED_PAD src0_sel:BYTE_3
	v_cvt_f32_i32_sdwa v13, sext(v89) dst_sel:DWORD dst_unused:UNUSED_PAD src0_sel:BYTE_1
	v_cvt_f32_i32_sdwa v12, sext(v89) dst_sel:DWORD dst_unused:UNUSED_PAD src0_sel:BYTE_0
	v_cvt_f32_i32_sdwa v10, sext(v89) dst_sel:DWORD dst_unused:UNUSED_PAD src0_sel:BYTE_2
	v_pk_add_f32 v[0:1], v[0:1], v[14:15]
	v_pk_add_f32 v[8:9], v[8:9], v[18:19]
	v_pk_add_f32 v[0:1], v[0:1], v[20:21]
	v_pk_add_f32 v[8:9], v[8:9], v[22:23]
	v_pk_mul_f32 v[0:1], v[0:1], s[10:11] op_sel_hi:[1,0]
	v_pk_mul_f32 v[8:9], v[8:9], s[10:11] op_sel_hi:[1,0]
	v_cvt_f32_fp8_e32 v14, v86
	v_pk_fma_f32 v[8:9], v[16:17], v[10:11], v[8:9] op_sel_hi:[0,1,1]
	v_pk_fma_f32 v[10:11], v[16:17], v[12:13], v[0:1] op_sel_hi:[0,1,1]
	v_cvt_f32_fp8_e32 v0, v85
	v_cvt_f32_fp8_sdwa v1, v85 src0_sel:BYTE_1
	v_cvt_f32_fp8_sdwa v12, v85 src0_sel:BYTE_2
	v_cvt_f32_fp8_sdwa v13, v85 src0_sel:BYTE_3
	v_cvt_f32_fp8_sdwa v15, v86 src0_sel:BYTE_1
	v_cvt_f32_fp8_sdwa v18, v86 src0_sel:BYTE_2
	v_cvt_f32_fp8_sdwa v19, v86 src0_sel:BYTE_3
	v_cvt_f32_fp8_e32 v20, v87
	v_cvt_f32_fp8_sdwa v21, v87 src0_sel:BYTE_1
	v_cvt_f32_fp8_sdwa v22, v87 src0_sel:BYTE_2
	v_cvt_f32_fp8_sdwa v23, v87 src0_sel:BYTE_3
	v_cvt_f32_fp8_e32 v36, v88
	v_cvt_f32_fp8_sdwa v37, v88 src0_sel:BYTE_1
	v_cvt_f32_fp8_sdwa v86, v88 src0_sel:BYTE_2
	v_cvt_f32_fp8_sdwa v87, v88 src0_sel:BYTE_3
	v_pk_add_f32 v[0:1], v[0:1], 0 op_sel_hi:[1,0]
	v_pk_add_f32 v[12:13], v[12:13], 0 op_sel_hi:[1,0]
	v_pk_add_f32 v[0:1], v[0:1], v[14:15]
	v_pk_add_f32 v[12:13], v[12:13], v[18:19]
	v_cvt_f32_i32_sdwa v15, sext(v84) dst_sel:DWORD dst_unused:UNUSED_PAD src0_sel:BYTE_3
	v_cvt_f32_i32_sdwa v19, sext(v84) dst_sel:DWORD dst_unused:UNUSED_PAD src0_sel:BYTE_1
	v_cvt_f32_i32_sdwa v18, sext(v84) dst_sel:DWORD dst_unused:UNUSED_PAD src0_sel:BYTE_0
	v_cvt_f32_i32_sdwa v14, sext(v84) dst_sel:DWORD dst_unused:UNUSED_PAD src0_sel:BYTE_2
	v_pk_add_f32 v[0:1], v[0:1], v[20:21]
	v_pk_add_f32 v[12:13], v[12:13], v[22:23]
	v_pk_add_f32 v[0:1], v[0:1], v[36:37]
	v_pk_add_f32 v[12:13], v[12:13], v[86:87]
	v_pk_mul_f32 v[0:1], v[0:1], s[10:11] op_sel_hi:[1,0]
	v_pk_mul_f32 v[12:13], v[12:13], s[10:11] op_sel_hi:[1,0]
	v_cvt_f32_fp8_e32 v20, v81
	v_pk_fma_f32 v[12:13], v[16:17], v[14:15], v[12:13] op_sel_hi:[0,1,1]
	v_pk_fma_f32 v[14:15], v[16:17], v[18:19], v[0:1] op_sel_hi:[0,1,1]
	v_cvt_f32_fp8_e32 v0, v80
	v_cvt_f32_fp8_sdwa v1, v80 src0_sel:BYTE_1
	v_cvt_f32_fp8_sdwa v18, v80 src0_sel:BYTE_2
	v_cvt_f32_fp8_sdwa v19, v80 src0_sel:BYTE_3
	v_cvt_f32_fp8_sdwa v21, v81 src0_sel:BYTE_1
	v_cvt_f32_fp8_sdwa v22, v81 src0_sel:BYTE_2
	v_cvt_f32_fp8_sdwa v23, v81 src0_sel:BYTE_3
	v_cvt_f32_fp8_e32 v36, v82
	v_cvt_f32_fp8_sdwa v37, v82 src0_sel:BYTE_1
	v_cvt_f32_fp8_sdwa v80, v82 src0_sel:BYTE_2
	v_cvt_f32_fp8_sdwa v81, v82 src0_sel:BYTE_3
	v_cvt_f32_fp8_e32 v84, v83
	v_cvt_f32_fp8_sdwa v85, v83 src0_sel:BYTE_1
	v_cvt_f32_fp8_sdwa v82, v83 src0_sel:BYTE_2
	v_cvt_f32_fp8_sdwa v83, v83 src0_sel:BYTE_3
	v_pk_add_f32 v[0:1], v[0:1], 0 op_sel_hi:[1,0]
	v_pk_add_f32 v[18:19], v[18:19], 0 op_sel_hi:[1,0]
	v_pk_add_f32 v[0:1], v[0:1], v[20:21]
	v_pk_add_f32 v[18:19], v[18:19], v[22:23]
; #define GAS __attribute__((address_space(1)))
; __device__ __forceinline__ void ln_row(f32x4 (&v)[4], const GAS float* g, const GAS float* b, int lane) {
;     ...
;     for (int j = 0; j < 4; ++j) s += (v[j].x + v[j].y) + (v[j].z + v[j].w);
;     const float mean = wave_sum(s) * (1.f / D); float s2 = 0.f;
; #pragma unroll
;     for (int j = 0; j < 4; ++j) { v[j] = v[j] - mean; s2 += (v[j].x * v[j].x + v[j].y * v[j].y) + (v[j].z * v[j].z + v[j].w * v[j].w); }
;     const float rstd = __builtin_amdgcn_rsqf(wave_sum(s2) * (1.f / D) + LN_EPS);
; #pragma unroll
;     for (int j = 0; j < 4; ++j) { const f32x4 gg = *(const GAS f32x4*)(g + 4 * lane + 256 * j), bb = *(const GAS f32x4*)(b + 4 * lane + 256 * j); v[j] = v[j] * rstd * gg + bb; }
; }
; __device__ __forceinline__ void p7_combine(Frame& F, int l) {
;     ...
;             ln_row(v[r], g2, b2, lane);
;             if (lastl) store_row_f(v[r], F.H + (size_t)(m + r) * D, lane);
	v_cvt_f32_i32_sdwa v21, sext(v38) dst_sel:DWORD dst_unused:UNUSED_PAD src0_sel:BYTE_3
	v_cvt_f32_i32_sdwa v23, sext(v38) dst_sel:DWORD dst_unused:UNUSED_PAD src0_sel:BYTE_1
	v_cvt_f32_i32_sdwa v22, sext(v38) dst_sel:DWORD dst_unused:UNUSED_PAD src0_sel:BYTE_0
	v_cvt_f32_i32_sdwa v20, sext(v38) dst_sel:DWORD dst_unused:UNUSED_PAD src0_sel:BYTE_2
	v_pk_add_f32 v[0:1], v[0:1], v[36:37]
	v_pk_add_f32 v[18:19], v[18:19], v[80:81]
	v_pk_add_f32 v[0:1], v[0:1], v[84:85]
	v_pk_add_f32 v[18:19], v[18:19], v[82:83]
	v_pk_mul_f32 v[36:37], v[0:1], s[10:11] op_sel_hi:[1,0]
	v_pk_mul_f32 v[0:1], v[18:19], s[10:11] op_sel_hi:[1,0]
	v_pk_fma_f32 v[36:37], v[16:17], v[22:23], v[36:37] op_sel_hi:[0,1,1]
	v_pk_fma_f32 v[0:1], v[16:17], v[20:21], v[0:1] op_sel_hi:[0,1,1]
	v_pk_mov_b32 v[16:17], v[6:7], v[4:5] op_sel:[1,0]
	v_mov_b32_e32 v18, v6
	v_mov_b32_e32 v19, v5
	v_pk_add_f32 v[16:17], v[16:17], v[18:19]
	v_pk_mov_b32 v[18:19], v[10:11], v[8:9] op_sel:[1,0]
	v_mov_b32_e32 v20, v10
	v_mov_b32_e32 v21, v9
	v_pk_add_f32 v[18:19], v[18:19], v[20:21]
	v_add_f32_e32 v16, v16, v17
	v_pk_add_f32 v[18:19], v[18:19], v[18:19] op_sel:[0,1] op_sel_hi:[1,0]
	v_add_f32_e32 v16, 0, v16
	v_add_f32_e32 v20, v14, v15
	v_add_f32_e32 v22, v12, v13
	v_mov_b32_e32 v17, v36
	v_mov_b32_e32 v19, v37
	v_mov_b32_e32 v21, v0
	v_mov_b32_e32 v23, v1
	v_pk_add_f32 v[16:17], v[16:17], v[18:19]
	v_pk_add_f32 v[18:19], v[20:21], v[22:23]
	s_and_b64 vcc, exec, s[36:37]
	v_pk_add_f32 v[16:17], v[16:17], v[18:19]
	s_nop 0
	v_add_f32_e32 v16, v16, v17
	v_mov_b32_e32 v17, v16
	s_nop 1
	v_mov_b32_dpp v17, v17 quad_perm:[1,0,3,2] row_mask:0xf bank_mask:0xf
	v_add_f32_e32 v16, v16, v17
	v_mov_b32_e32 v17, v16
	s_nop 1
	v_mov_b32_dpp v17, v17 quad_perm:[2,3,0,1] row_mask:0xf bank_mask:0xf
	v_add_f32_e32 v16, v16, v17
	v_mov_b32_e32 v17, v16
	s_nop 1
	v_mov_b32_dpp v17, v17 row_ror:4 row_mask:0xf bank_mask:0xf
	v_add_f32_e32 v16, v16, v17
	v_mov_b32_e32 v17, v16
	s_nop 1
	v_mov_b32_dpp v17, v17 row_ror:8 row_mask:0xf bank_mask:0xf
	v_add_f32_e32 v16, v16, v17
	v_mov_b32_e32 v17, v16
	s_nop 1
	v_mov_b32_dpp v17, v17 row_bcast:15 row_mask:0xa bank_mask:0xf
	v_add_f32_e32 v16, v16, v17
	v_mov_b32_e32 v17, v16
	s_nop 1
	v_mov_b32_dpp v17, v17 row_bcast:31 row_mask:0xc bank_mask:0xf
	v_add_f32_e32 v16, v16, v17
	s_nop 0
	v_readlane_b32 s10, v16, 63
	s_nop 1
	v_fma_f32 v7, s10, v196, v7
	v_fmac_f32_e32 v6, s10, v196
	v_fma_f32 v5, s10, v196, v5
	v_fmac_f32_e32 v4, s10, v196
	v_pk_mul_f32 v[16:17], v[4:5], v[4:5]
	v_pk_mul_f32 v[18:19], v[6:7], v[6:7]
	v_fma_f32 v11, s10, v196, v11
	v_pk_mov_b32 v[20:21], v[18:19], v[16:17] op_sel:[1,0]
	v_mov_b32_e32 v19, v17
	v_pk_add_f32 v[16:17], v[20:21], v[18:19]
	v_fmac_f32_e32 v10, s10, v196
	v_fma_f32 v9, s10, v196, v9
	v_fmac_f32_e32 v8, s10, v196
	v_pk_add_f32 v[16:17], v[16:17], v[16:17] op_sel_hi:[0,1]
	v_pk_mul_f32 v[18:19], v[8:9], v[8:9]
	v_pk_mul_f32 v[20:21], v[10:11], v[10:11]
	v_fmac_f32_e32 v14, s10, v196
	v_pk_mov_b32 v[22:23], v[20:21], v[18:19] op_sel:[1,0]
	v_mov_b32_e32 v21, v19
	v_fma_f32 v15, s10, v196, v15
	v_fmac_f32_e32 v12, s10, v196
	v_mul_f32_e32 v16, v14, v14
	v_pk_add_f32 v[18:19], v[22:23], v[20:21]
	v_fma_f32 v13, s10, v196, v13
	v_pk_fma_f32 v[20:21], v[14:15], v[14:15], v[16:17] op_sel_hi:[1,1,0]
	v_mul_f32_e32 v16, v12, v12
	v_pk_add_f32 v[18:19], v[18:19], v[18:19] op_sel_hi:[0,1]
	v_pk_fma_f32 v[22:23], v[12:13], v[12:13], v[16:17] op_sel_hi:[1,1,0]
	v_fma_f32 v1, s10, v196, v1
	v_fmac_f32_e32 v0, s10, v196
	v_fma_f32 v37, s10, v196, v37
	v_fmac_f32_e32 v36, s10, v196
	v_mul_f32_e32 v20, v36, v36
	v_mul_f32_e32 v22, v37, v37
	v_mul_f32_e32 v16, v0, v0
	v_mul_f32_e32 v18, v1, v1
	v_pk_add_f32 v[20:21], v[20:21], v[22:23]
	v_pk_add_f32 v[16:17], v[16:17], v[18:19]
	s_nop 0
	v_pk_add_f32 v[16:17], v[20:21], v[16:17]
	s_nop 0
	v_add_f32_e32 v16, v16, v17
	v_mov_b32_e32 v17, v16
	s_nop 1
	v_mov_b32_dpp v17, v17 quad_perm:[1,0,3,2] row_mask:0xf bank_mask:0xf
	v_add_f32_e32 v16, v16, v17
	v_mov_b32_e32 v17, v16
	s_nop 1
	v_mov_b32_dpp v17, v17 quad_perm:[2,3,0,1] row_mask:0xf bank_mask:0xf
	v_add_f32_e32 v16, v16, v17
	v_mov_b32_e32 v17, v16
	s_nop 1
	v_mov_b32_dpp v17, v17 row_ror:4 row_mask:0xf bank_mask:0xf
	v_add_f32_e32 v16, v16, v17
	v_mov_b32_e32 v17, v16
	s_nop 1
	v_mov_b32_dpp v17, v17 row_ror:8 row_mask:0xf bank_mask:0xf
	v_add_f32_e32 v16, v16, v17
	v_mov_b32_e32 v17, v16
	s_nop 1
	v_mov_b32_dpp v17, v17 row_bcast:15 row_mask:0xa bank_mask:0xf
	v_add_f32_e32 v16, v16, v17
	v_mov_b32_e32 v17, v16
	s_nop 1
	v_mov_b32_dpp v17, v17 row_bcast:31 row_mask:0xc bank_mask:0xf
	v_add_f32_e32 v16, v16, v17
	s_nop 0
	v_readlane_b32 s10, v16, 63
	s_nop 1
	v_fma_f32 v16, s10, v197, v190
	v_rsq_f32_e32 v38, v16
	s_nop 1
	s_mov_b64 s[10:11], -1
	v_pk_mul_f32 v[80:81], v[6:7], v[38:39] op_sel_hi:[1,0]
	v_pk_mul_f32 v[4:5], v[4:5], v[38:39] op_sel_hi:[1,0]
	v_pk_mul_f32 v[8:9], v[8:9], v[38:39] op_sel_hi:[1,0]
	v_pk_mul_f32 v[12:13], v[12:13], v[38:39] op_sel_hi:[1,0]
	v_pk_mul_f32 v[36:37], v[36:37], v[38:39] op_sel_hi:[1,0]
	v_pk_mul_f32 v[0:1], v[0:1], v[38:39] op_sel_hi:[1,0]
	s_nop 0
	v_pk_fma_f32 v[6:7], v[206:207], v[4:5], v[222:223]
	v_pk_fma_f32 v[4:5], v[204:205], v[80:81], v[220:221]
	s_nop 1
	v_pk_mul_f32 v[80:81], v[10:11], v[38:39] op_sel_hi:[1,0]
	s_nop 0
	v_pk_fma_f32 v[10:11], v[210:211], v[8:9], v[226:227]
	v_pk_fma_f32 v[8:9], v[208:209], v[80:81], v[224:225]
	s_nop 1
	v_pk_mul_f32 v[80:81], v[14:15], v[38:39] op_sel_hi:[1,0]
	s_nop 0
	v_pk_fma_f32 v[14:15], v[214:215], v[12:13], v[230:231]
	v_pk_fma_f32 v[12:13], v[212:213], v[80:81], v[228:229]
	s_nop 1
	s_nop 0
	v_pk_fma_f32 v[18:19], v[0:1], v[218:219], v[234:235]
	v_pk_fma_f32 v[16:17], v[36:37], v[216:217], v[232:233]
	s_cbranch_vccnz .LBB0_1063
	v_add_co_u32_e32 v0, vcc, 0x1000, v34
	s_mov_b64 s[10:11], 0
	s_nop 0
	v_addc_co_u32_e32 v1, vcc, 0, v35, vcc
	global_store_dwordx4 v[0:1], v[4:7], off
	global_store_dwordx4 v[0:1], v[8:11], off offset:1024
	global_store_dwordx4 v[0:1], v[12:15], off offset:2048
	global_store_dwordx4 v[0:1], v[16:19], off offset:3072

; __device__ __forceinline__ void p7_combine(Frame& F, int l) {
;     ...
;         for (int r = 0; r < 4; ++r) {
; #pragma unroll
;             for (int j = 0; j < 4; ++j) { const int hw = (int)hv[r][j]; f32x4 a; a.x = (float)((hw << 24) >> 24) * hsa[r]; a.y = (float)((hw << 16) >> 24) * hsa[r]; a.z = (float)((hw << 8) >> 24) * hsa[r]; a.w = (float)(hw >> 24) * hsa[r];
;                 f32x4 ys = (f32x4){0.f, 0.f, 0.f, 0.f};
; #pragma unroll
;                 for (int k = 0; k < 4; ++k) { const int w = (int)yv[r][k][j]; ys.x += __builtin_amdgcn_cvt_f32_fp8(w, 0); ys.y += __builtin_amdgcn_cvt_f32_fp8(w, 1); ys.z += __builtin_amdgcn_cvt_f32_fp8(w, 2); ys.w += __builtin_amdgcn_cvt_f32_fp8(w, 3); }
;                 v[r][j] = a + ys * (1.0f / 16.0f); }
.LBB0_1067:
	s_waitcnt vmcnt(28)
	v_cvt_f32_fp8_e32 v0, v76
	v_cvt_f32_fp8_sdwa v1, v76 src0_sel:BYTE_1
	v_cvt_f32_fp8_sdwa v4, v76 src0_sel:BYTE_2
	v_cvt_f32_fp8_sdwa v5, v76 src0_sel:BYTE_3
	v_cvt_f32_fp8_e32 v6, v77
	v_cvt_f32_fp8_sdwa v7, v77 src0_sel:BYTE_1
	v_cvt_f32_fp8_sdwa v8, v77 src0_sel:BYTE_2
	v_cvt_f32_fp8_sdwa v9, v77 src0_sel:BYTE_3
	v_cvt_f32_fp8_e32 v10, v78
	v_cvt_f32_fp8_sdwa v11, v78 src0_sel:BYTE_1
	v_cvt_f32_fp8_sdwa v12, v78 src0_sel:BYTE_2
	v_cvt_f32_fp8_sdwa v13, v78 src0_sel:BYTE_3
	v_cvt_f32_fp8_e32 v14, v79
	v_cvt_f32_fp8_sdwa v15, v79 src0_sel:BYTE_1
	v_cvt_f32_fp8_sdwa v16, v79 src0_sel:BYTE_2
	v_cvt_f32_fp8_sdwa v17, v79 src0_sel:BYTE_3
	v_pk_add_f32 v[0:1], v[0:1], 0 op_sel_hi:[1,0]
	v_pk_add_f32 v[4:5], v[4:5], 0 op_sel_hi:[1,0]
	v_pk_add_f32 v[0:1], v[0:1], v[6:7]
	v_pk_add_f32 v[4:5], v[4:5], v[8:9]
	v_cvt_f32_i32_sdwa v7, sext(v75) dst_sel:DWORD dst_unused:UNUSED_PAD src0_sel:BYTE_3
	v_cvt_f32_i32_sdwa v9, sext(v75) dst_sel:DWORD dst_unused:UNUSED_PAD src0_sel:BYTE_1
	v_cvt_f32_i32_sdwa v8, sext(v75) dst_sel:DWORD dst_unused:UNUSED_PAD src0_sel:BYTE_0
	v_cvt_f32_i32_sdwa v6, sext(v75) dst_sel:DWORD dst_unused:UNUSED_PAD src0_sel:BYTE_2
	v_pk_add_f32 v[0:1], v[0:1], v[10:11]
	v_pk_add_f32 v[4:5], v[4:5], v[12:13]
	v_pk_add_f32 v[0:1], v[0:1], v[14:15]
	v_pk_add_f32 v[4:5], v[4:5], v[16:17]
	s_mov_b32 s10, 0x3d800000
	v_mul_f32_e32 v2, 0x3fb504f3, v2
	v_pk_mul_f32 v[0:1], v[0:1], s[10:11] op_sel_hi:[1,0]
	v_pk_mul_f32 v[4:5], v[4:5], s[10:11] op_sel_hi:[1,0]
	v_cvt_f32_fp8_e32 v10, v72
	v_pk_fma_f32 v[4:5], v[2:3], v[6:7], v[4:5] op_sel_hi:[0,1,1]
	v_pk_fma_f32 v[6:7], v[2:3], v[8:9], v[0:1] op_sel_hi:[0,1,1]
	v_cvt_f32_fp8_e32 v0, v71
	v_cvt_f32_fp8_sdwa v1, v71 src0_sel:BYTE_1
	v_cvt_f32_fp8_sdwa v8, v71 src0_sel:BYTE_2
	v_cvt_f32_fp8_sdwa v9, v71 src0_sel:BYTE_3
	v_cvt_f32_fp8_sdwa v11, v72 src0_sel:BYTE_1
	v_cvt_f32_fp8_sdwa v12, v72 src0_sel:BYTE_2
	v_cvt_f32_fp8_sdwa v13, v72 src0_sel:BYTE_3
	v_cvt_f32_fp8_e32 v14, v73
	v_cvt_f32_fp8_sdwa v15, v73 src0_sel:BYTE_1
	v_cvt_f32_fp8_sdwa v16, v73 src0_sel:BYTE_2
	v_cvt_f32_fp8_sdwa v17, v73 src0_sel:BYTE_3
	v_cvt_f32_fp8_e32 v18, v74
	v_cvt_f32_fp8_sdwa v19, v74 src0_sel:BYTE_1
	v_cvt_f32_fp8_sdwa v20, v74 src0_sel:BYTE_2
	v_cvt_f32_fp8_sdwa v21, v74 src0_sel:BYTE_3
	v_pk_add_f32 v[0:1], v[0:1], 0 op_sel_hi:[1,0]
	v_pk_add_f32 v[8:9], v[8:9], 0 op_sel_hi:[1,0]
	v_pk_add_f32 v[0:1], v[0:1], v[10:11]
	v_pk_add_f32 v[8:9], v[8:9], v[12:13]
	v_cvt_f32_i32_sdwa v11, sext(v70) dst_sel:DWORD dst_unused:UNUSED_PAD src0_sel:BYTE_3
	v_cvt_f32_i32_sdwa v13, sext(v70) dst_sel:DWORD dst_unused:UNUSED_PAD src0_sel:BYTE_1
	v_cvt_f32_i32_sdwa v12, sext(v70) dst_sel:DWORD dst_unused:UNUSED_PAD src0_sel:BYTE_0
	v_cvt_f32_i32_sdwa v10, sext(v70) dst_sel:DWORD dst_unused:UNUSED_PAD src0_sel:BYTE_2
	v_pk_add_f32 v[0:1], v[0:1], v[14:15]
	v_pk_add_f32 v[8:9], v[8:9], v[16:17]
	v_pk_add_f32 v[0:1], v[0:1], v[18:19]
	v_pk_add_f32 v[8:9], v[8:9], v[20:21]
	v_pk_mul_f32 v[0:1], v[0:1], s[10:11] op_sel_hi:[1,0]
	v_pk_mul_f32 v[8:9], v[8:9], s[10:11] op_sel_hi:[1,0]
	v_cvt_f32_fp8_e32 v14, v67
	v_pk_fma_f32 v[8:9], v[2:3], v[10:11], v[8:9] op_sel_hi:[0,1,1]
	v_pk_fma_f32 v[10:11], v[2:3], v[12:13], v[0:1] op_sel_hi:[0,1,1]
	v_cvt_f32_fp8_e32 v0, v66
	v_cvt_f32_fp8_sdwa v1, v66 src0_sel:BYTE_1
	v_cvt_f32_fp8_sdwa v12, v66 src0_sel:BYTE_2
	v_cvt_f32_fp8_sdwa v13, v66 src0_sel:BYTE_3
	v_cvt_f32_fp8_sdwa v15, v67 src0_sel:BYTE_1
	v_cvt_f32_fp8_sdwa v16, v67 src0_sel:BYTE_2
	v_cvt_f32_fp8_sdwa v17, v67 src0_sel:BYTE_3
	v_cvt_f32_fp8_e32 v18, v68
	v_cvt_f32_fp8_sdwa v19, v68 src0_sel:BYTE_1
	v_cvt_f32_fp8_sdwa v20, v68 src0_sel:BYTE_2
	v_cvt_f32_fp8_sdwa v21, v68 src0_sel:BYTE_3
	v_cvt_f32_fp8_e32 v22, v69
	v_cvt_f32_fp8_sdwa v23, v69 src0_sel:BYTE_1
	v_cvt_f32_fp8_sdwa v36, v69 src0_sel:BYTE_2
	v_cvt_f32_fp8_sdwa v37, v69 src0_sel:BYTE_3
	v_pk_add_f32 v[0:1], v[0:1], 0 op_sel_hi:[1,0]
	v_pk_add_f32 v[12:13], v[12:13], 0 op_sel_hi:[1,0]
	v_pk_add_f32 v[0:1], v[0:1], v[14:15]
	v_pk_add_f32 v[12:13], v[12:13], v[16:17]
	v_cvt_f32_i32_sdwa v15, sext(v65) dst_sel:DWORD dst_unused:UNUSED_PAD src0_sel:BYTE_3
	v_cvt_f32_i32_sdwa v17, sext(v65) dst_sel:DWORD dst_unused:UNUSED_PAD src0_sel:BYTE_1
	v_cvt_f32_i32_sdwa v16, sext(v65) dst_sel:DWORD dst_unused:UNUSED_PAD src0_sel:BYTE_0
	v_cvt_f32_i32_sdwa v14, sext(v65) dst_sel:DWORD dst_unused:UNUSED_PAD src0_sel:BYTE_2
	v_pk_add_f32 v[0:1], v[0:1], v[18:19]
	v_pk_add_f32 v[12:13], v[12:13], v[20:21]
	v_pk_add_f32 v[0:1], v[0:1], v[22:23]
	v_pk_add_f32 v[12:13], v[12:13], v[36:37]
	v_pk_mul_f32 v[0:1], v[0:1], s[10:11] op_sel_hi:[1,0]
	v_pk_mul_f32 v[12:13], v[12:13], s[10:11] op_sel_hi:[1,0]
	v_cvt_f32_fp8_e32 v18, v62
	v_pk_fma_f32 v[12:13], v[2:3], v[14:15], v[12:13] op_sel_hi:[0,1,1]
	v_pk_fma_f32 v[14:15], v[2:3], v[16:17], v[0:1] op_sel_hi:[0,1,1]
	v_cvt_f32_fp8_e32 v0, v61
	v_cvt_f32_fp8_sdwa v1, v61 src0_sel:BYTE_1
	v_cvt_f32_fp8_sdwa v16, v61 src0_sel:BYTE_2
	v_cvt_f32_fp8_sdwa v17, v61 src0_sel:BYTE_3
	v_cvt_f32_fp8_sdwa v19, v62 src0_sel:BYTE_1
	v_cvt_f32_fp8_sdwa v20, v62 src0_sel:BYTE_2
	v_cvt_f32_fp8_sdwa v21, v62 src0_sel:BYTE_3
	v_cvt_f32_fp8_e32 v22, v63
	v_cvt_f32_fp8_sdwa v23, v63 src0_sel:BYTE_1
	v_cvt_f32_fp8_sdwa v36, v63 src0_sel:BYTE_2
	v_cvt_f32_fp8_sdwa v37, v63 src0_sel:BYTE_3
	v_cvt_f32_fp8_e32 v62, v64
	v_cvt_f32_fp8_sdwa v63, v64 src0_sel:BYTE_1
	v_cvt_f32_fp8_sdwa v66, v64 src0_sel:BYTE_2
	v_cvt_f32_fp8_sdwa v67, v64 src0_sel:BYTE_3
	v_pk_add_f32 v[0:1], v[0:1], 0 op_sel_hi:[1,0]
	v_pk_add_f32 v[16:17], v[16:17], 0 op_sel_hi:[1,0]
	v_pk_add_f32 v[0:1], v[0:1], v[18:19]
	v_pk_add_f32 v[16:17], v[16:17], v[20:21]
; #define GAS __attribute__((address_space(1)))
; __device__ __forceinline__ void ln_row(f32x4 (&v)[4], const GAS float* g, const GAS float* b, int lane) {
;     ...
;     for (int j = 0; j < 4; ++j) s += (v[j].x + v[j].y) + (v[j].z + v[j].w);
;     const float mean = wave_sum(s) * (1.f / D); float s2 = 0.f;
; #pragma unroll
;     for (int j = 0; j < 4; ++j) { v[j] = v[j] - mean; s2 += (v[j].x * v[j].x + v[j].y * v[j].y) + (v[j].z * v[j].z + v[j].w * v[j].w); }
;     const float rstd = __builtin_amdgcn_rsqf(wave_sum(s2) * (1.f / D) + LN_EPS);
; #pragma unroll
;     for (int j = 0; j < 4; ++j) { const f32x4 gg = *(const GAS f32x4*)(g + 4 * lane + 256 * j), bb = *(const GAS f32x4*)(b + 4 * lane + 256 * j); v[j] = v[j] * rstd * gg + bb; }
; }
; __device__ __forceinline__ void p7_combine(Frame& F, int l) {
;     ...
;             ln_row(v[r], g2, b2, lane);
;             if (lastl) store_row_f(v[r], F.H + (size_t)(m + r) * D, lane);
	v_cvt_f32_i32_sdwa v19, sext(v60) dst_sel:DWORD dst_unused:UNUSED_PAD src0_sel:BYTE_3
	v_cvt_f32_i32_sdwa v18, sext(v60) dst_sel:DWORD dst_unused:UNUSED_PAD src0_sel:BYTE_2
	v_pk_add_f32 v[0:1], v[0:1], v[22:23]
	v_pk_add_f32 v[16:17], v[16:17], v[36:37]
	v_cvt_f32_i32_sdwa v21, sext(v60) dst_sel:DWORD dst_unused:UNUSED_PAD src0_sel:BYTE_1
	v_cvt_f32_i32_sdwa v20, sext(v60) dst_sel:DWORD dst_unused:UNUSED_PAD src0_sel:BYTE_0
	v_pk_add_f32 v[16:17], v[16:17], v[66:67]
	v_pk_add_f32 v[0:1], v[0:1], v[62:63]
	s_and_b64 vcc, exec, s[36:37]
	v_pk_mul_f32 v[22:23], v[0:1], s[10:11] op_sel_hi:[1,0]
	v_pk_mul_f32 v[0:1], v[16:17], s[10:11] op_sel_hi:[1,0]
	v_pk_mov_b32 v[16:17], v[6:7], v[4:5] op_sel:[1,0]
	v_pk_fma_f32 v[0:1], v[2:3], v[18:19], v[0:1] op_sel_hi:[0,1,1]
	v_mov_b32_e32 v18, v6
	v_mov_b32_e32 v19, v5
	v_pk_fma_f32 v[36:37], v[2:3], v[20:21], v[22:23] op_sel_hi:[0,1,1]
	v_pk_add_f32 v[16:17], v[16:17], v[18:19]
	v_pk_mov_b32 v[18:19], v[10:11], v[8:9] op_sel:[1,0]
	v_mov_b32_e32 v20, v10
	v_mov_b32_e32 v21, v9
	v_pk_add_f32 v[18:19], v[18:19], v[20:21]
	v_add_f32_e32 v2, v16, v17
	v_pk_add_f32 v[18:19], v[18:19], v[18:19] op_sel:[0,1] op_sel_hi:[1,0]
	v_add_f32_e32 v16, 0, v2
	v_add_f32_e32 v20, v14, v15
	v_add_f32_e32 v22, v12, v13
	v_mov_b32_e32 v17, v36
	v_mov_b32_e32 v19, v37
	v_mov_b32_e32 v21, v0
	v_mov_b32_e32 v23, v1
	v_pk_add_f32 v[16:17], v[16:17], v[18:19]
	v_pk_add_f32 v[18:19], v[20:21], v[22:23]
	s_nop 0
	v_pk_add_f32 v[16:17], v[16:17], v[18:19]
	s_nop 0
	v_add_f32_e32 v2, v16, v17
	v_mov_b32_e32 v16, v2
	s_nop 1
	v_mov_b32_dpp v16, v16 quad_perm:[1,0,3,2] row_mask:0xf bank_mask:0xf
	v_add_f32_e32 v2, v2, v16
	v_mov_b32_e32 v16, v2
	s_nop 1
	v_mov_b32_dpp v16, v16 quad_perm:[2,3,0,1] row_mask:0xf bank_mask:0xf
	v_add_f32_e32 v2, v2, v16
	v_mov_b32_e32 v16, v2
	s_nop 1
	v_mov_b32_dpp v16, v16 row_ror:4 row_mask:0xf bank_mask:0xf
	v_add_f32_e32 v2, v2, v16
	v_mov_b32_e32 v16, v2
	s_nop 1
	v_mov_b32_dpp v16, v16 row_ror:8 row_mask:0xf bank_mask:0xf
	v_add_f32_e32 v2, v2, v16
	v_mov_b32_e32 v16, v2
	s_nop 1
	v_mov_b32_dpp v16, v16 row_bcast:15 row_mask:0xa bank_mask:0xf
	v_add_f32_e32 v2, v2, v16
	v_mov_b32_e32 v16, v2
	s_nop 1
	v_mov_b32_dpp v16, v16 row_bcast:31 row_mask:0xc bank_mask:0xf
	v_add_f32_e32 v2, v2, v16
	s_nop 0
	v_readlane_b32 s10, v2, 63
	s_nop 1
	v_fma_f32 v7, s10, v196, v7
	v_fmac_f32_e32 v6, s10, v196
	v_fma_f32 v5, s10, v196, v5
	v_fmac_f32_e32 v4, s10, v196
	v_pk_mul_f32 v[16:17], v[4:5], v[4:5]
	v_pk_mul_f32 v[18:19], v[6:7], v[6:7]
	v_fma_f32 v11, s10, v196, v11
	v_pk_mov_b32 v[20:21], v[18:19], v[16:17] op_sel:[1,0]
	v_mov_b32_e32 v19, v17
	v_fmac_f32_e32 v10, s10, v196
	v_fma_f32 v9, s10, v196, v9
	v_fmac_f32_e32 v8, s10, v196
	v_pk_add_f32 v[16:17], v[20:21], v[18:19]
	v_pk_mul_f32 v[18:19], v[8:9], v[8:9]
	v_pk_mul_f32 v[20:21], v[10:11], v[10:11]
	v_fmac_f32_e32 v14, s10, v196
	v_pk_mov_b32 v[22:23], v[20:21], v[18:19] op_sel:[1,0]
	v_mov_b32_e32 v21, v19
	v_fma_f32 v15, s10, v196, v15
	v_fmac_f32_e32 v12, s10, v196
	v_mul_f32_e32 v2, v14, v14
	v_pk_add_f32 v[18:19], v[22:23], v[20:21]
	v_fma_f32 v13, s10, v196, v13
	v_pk_fma_f32 v[20:21], v[14:15], v[14:15], v[2:3] op_sel_hi:[1,1,0]
	v_mul_f32_e32 v2, v12, v12
	v_pk_add_f32 v[16:17], v[16:17], v[16:17] op_sel_hi:[0,1]
	v_pk_add_f32 v[18:19], v[18:19], v[18:19] op_sel_hi:[0,1]
	v_pk_fma_f32 v[22:23], v[12:13], v[12:13], v[2:3] op_sel_hi:[1,1,0]
	v_fma_f32 v1, s10, v196, v1
	v_fmac_f32_e32 v0, s10, v196
	v_fma_f32 v37, s10, v196, v37
	v_fmac_f32_e32 v36, s10, v196
	v_mul_f32_e32 v20, v36, v36
	v_mul_f32_e32 v22, v37, v37
	v_mul_f32_e32 v16, v0, v0
	v_mul_f32_e32 v18, v1, v1
	v_pk_add_f32 v[20:21], v[20:21], v[22:23]
	v_pk_add_f32 v[16:17], v[16:17], v[18:19]
	s_nop 0
	v_pk_add_f32 v[16:17], v[20:21], v[16:17]
	s_nop 0
	v_add_f32_e32 v2, v16, v17
	v_mov_b32_e32 v16, v2
	s_nop 1
	v_mov_b32_dpp v16, v16 quad_perm:[1,0,3,2] row_mask:0xf bank_mask:0xf
	v_add_f32_e32 v2, v2, v16
	v_mov_b32_e32 v16, v2
	s_nop 1
	v_mov_b32_dpp v16, v16 quad_perm:[2,3,0,1] row_mask:0xf bank_mask:0xf
	v_add_f32_e32 v2, v2, v16
	v_mov_b32_e32 v16, v2
	s_nop 1
	v_mov_b32_dpp v16, v16 row_ror:4 row_mask:0xf bank_mask:0xf
	v_add_f32_e32 v2, v2, v16
	v_mov_b32_e32 v16, v2
	s_nop 1
	v_mov_b32_dpp v16, v16 row_ror:8 row_mask:0xf bank_mask:0xf
	v_add_f32_e32 v2, v2, v16
	v_mov_b32_e32 v16, v2
	s_nop 1
	v_mov_b32_dpp v16, v16 row_bcast:15 row_mask:0xa bank_mask:0xf
	v_add_f32_e32 v2, v2, v16
	v_mov_b32_e32 v16, v2
	s_nop 1
	v_mov_b32_dpp v16, v16 row_bcast:31 row_mask:0xc bank_mask:0xf
	v_add_f32_e32 v2, v2, v16
	s_nop 1
	v_readlane_b32 s10, v2, 63
	s_nop 1
	v_fma_f32 v2, s10, v197, v190
	v_rsq_f32_e32 v2, v2
	s_mov_b64 s[10:11], -1
	v_pk_mul_f32 v[60:61], v[6:7], v[2:3] op_sel_hi:[1,0]
	v_pk_mul_f32 v[4:5], v[4:5], v[2:3] op_sel_hi:[1,0]
	v_pk_mul_f32 v[8:9], v[8:9], v[2:3] op_sel_hi:[1,0]
	v_pk_mul_f32 v[12:13], v[12:13], v[2:3] op_sel_hi:[1,0]
	v_pk_mul_f32 v[36:37], v[36:37], v[2:3] op_sel_hi:[1,0]
	v_pk_mul_f32 v[0:1], v[0:1], v[2:3] op_sel_hi:[1,0]
	s_nop 0
	v_pk_fma_f32 v[6:7], v[206:207], v[4:5], v[222:223]
	v_pk_fma_f32 v[4:5], v[204:205], v[60:61], v[220:221]
	s_nop 1
	v_pk_mul_f32 v[60:61], v[10:11], v[2:3] op_sel_hi:[1,0]
	s_nop 0
	v_pk_fma_f32 v[10:11], v[210:211], v[8:9], v[226:227]
	v_pk_fma_f32 v[8:9], v[208:209], v[60:61], v[224:225]
	s_nop 1
	v_pk_mul_f32 v[60:61], v[14:15], v[2:3] op_sel_hi:[1,0]
	s_nop 0
	v_pk_fma_f32 v[14:15], v[214:215], v[12:13], v[230:231]
	v_pk_fma_f32 v[12:13], v[212:213], v[60:61], v[228:229]
	s_nop 1
	s_nop 0
	v_pk_fma_f32 v[18:19], v[0:1], v[218:219], v[234:235]
	v_pk_fma_f32 v[16:17], v[36:37], v[216:217], v[232:233]
	s_cbranch_vccnz .LBB0_1069
	v_add_co_u32_e32 v0, vcc, 0x2000, v34
	s_mov_b64 s[10:11], 0
	s_nop 0
	v_addc_co_u32_e32 v1, vcc, 0, v35, vcc
	global_store_dwordx4 v[0:1], v[4:7], off
	global_store_dwordx4 v[0:1], v[8:11], off offset:1024
	global_store_dwordx4 v[0:1], v[12:15], off offset:2048
	global_store_dwordx4 v[0:1], v[16:19], off offset:3072

; __device__ __forceinline__ void p7_combine(Frame& F, int l) {
;     ...
;         for (int r = 0; r < 4; ++r) {
; #pragma unroll
;             for (int j = 0; j < 4; ++j) { const int hw = (int)hv[r][j]; f32x4 a; a.x = (float)((hw << 24) >> 24) * hsa[r]; a.y = (float)((hw << 16) >> 24) * hsa[r]; a.z = (float)((hw << 8) >> 24) * hsa[r]; a.w = (float)(hw >> 24) * hsa[r];
;                 f32x4 ys = (f32x4){0.f, 0.f, 0.f, 0.f};
; #pragma unroll
;                 for (int k = 0; k < 4; ++k) { const int w = (int)yv[r][k][j]; ys.x += __builtin_amdgcn_cvt_f32_fp8(w, 0); ys.y += __builtin_amdgcn_cvt_f32_fp8(w, 1); ys.z += __builtin_amdgcn_cvt_f32_fp8(w, 2); ys.w += __builtin_amdgcn_cvt_f32_fp8(w, 3); }
;                 v[r][j] = a + ys * (1.0f / 16.0f); }
.LBB0_1073:
	s_waitcnt vmcnt(12)
	v_mul_f32_e32 v12, 0x3fb504f3, v3
	v_cvt_f32_fp8_e32 v0, v56
	v_cvt_f32_fp8_sdwa v1, v56 src0_sel:BYTE_1
	v_cvt_f32_fp8_sdwa v2, v56 src0_sel:BYTE_2
	v_cvt_f32_fp8_sdwa v3, v56 src0_sel:BYTE_3
	v_cvt_f32_fp8_e32 v4, v57
	v_cvt_f32_fp8_sdwa v5, v57 src0_sel:BYTE_1
	v_cvt_f32_fp8_sdwa v6, v57 src0_sel:BYTE_2
	v_cvt_f32_fp8_sdwa v7, v57 src0_sel:BYTE_3
	v_cvt_f32_fp8_e32 v8, v58
	v_cvt_f32_fp8_sdwa v9, v58 src0_sel:BYTE_1
	v_cvt_f32_fp8_sdwa v10, v58 src0_sel:BYTE_2
	v_cvt_f32_fp8_sdwa v11, v58 src0_sel:BYTE_3
	v_cvt_f32_fp8_e32 v14, v59
	v_cvt_f32_fp8_sdwa v15, v59 src0_sel:BYTE_1
	v_cvt_f32_fp8_sdwa v16, v59 src0_sel:BYTE_2
	v_cvt_f32_fp8_sdwa v17, v59 src0_sel:BYTE_3
	v_pk_add_f32 v[0:1], v[0:1], 0 op_sel_hi:[1,0]
	v_pk_add_f32 v[2:3], v[2:3], 0 op_sel_hi:[1,0]
	v_pk_add_f32 v[0:1], v[0:1], v[4:5]
	v_pk_add_f32 v[2:3], v[2:3], v[6:7]
	v_cvt_f32_i32_sdwa v5, sext(v43) dst_sel:DWORD dst_unused:UNUSED_PAD src0_sel:BYTE_3
	v_cvt_f32_i32_sdwa v7, sext(v43) dst_sel:DWORD dst_unused:UNUSED_PAD src0_sel:BYTE_1
	v_cvt_f32_i32_sdwa v6, sext(v43) dst_sel:DWORD dst_unused:UNUSED_PAD src0_sel:BYTE_0
	v_cvt_f32_i32_sdwa v4, sext(v43) dst_sel:DWORD dst_unused:UNUSED_PAD src0_sel:BYTE_2
	v_pk_add_f32 v[0:1], v[0:1], v[8:9]
	v_pk_add_f32 v[2:3], v[2:3], v[10:11]
	v_pk_add_f32 v[0:1], v[0:1], v[14:15]
	v_pk_add_f32 v[2:3], v[2:3], v[16:17]
	s_mov_b32 s10, 0x3d800000
	v_pk_mul_f32 v[8:9], v[0:1], s[10:11] op_sel_hi:[1,0]
	v_pk_mul_f32 v[0:1], v[2:3], s[10:11] op_sel_hi:[1,0]
	v_pk_fma_f32 v[2:3], v[12:13], v[6:7], v[8:9] op_sel_hi:[0,1,1]
	v_pk_fma_f32 v[0:1], v[12:13], v[4:5], v[0:1] op_sel_hi:[0,1,1]
	v_cvt_f32_fp8_e32 v4, v52
	v_cvt_f32_fp8_sdwa v5, v52 src0_sel:BYTE_1
	v_cvt_f32_fp8_sdwa v6, v52 src0_sel:BYTE_2
	v_cvt_f32_fp8_sdwa v7, v52 src0_sel:BYTE_3
	v_cvt_f32_fp8_e32 v8, v53
	v_cvt_f32_fp8_sdwa v9, v53 src0_sel:BYTE_1
	v_cvt_f32_fp8_sdwa v10, v53 src0_sel:BYTE_2
	v_cvt_f32_fp8_sdwa v11, v53 src0_sel:BYTE_3
	v_cvt_f32_fp8_e32 v14, v54
	v_cvt_f32_fp8_sdwa v15, v54 src0_sel:BYTE_1
	v_cvt_f32_fp8_sdwa v16, v54 src0_sel:BYTE_2
	v_cvt_f32_fp8_sdwa v17, v54 src0_sel:BYTE_3
	v_cvt_f32_fp8_e32 v18, v55
	v_cvt_f32_fp8_sdwa v19, v55 src0_sel:BYTE_1
	v_cvt_f32_fp8_sdwa v20, v55 src0_sel:BYTE_2
	v_cvt_f32_fp8_sdwa v21, v55 src0_sel:BYTE_3
	v_pk_add_f32 v[4:5], v[4:5], 0 op_sel_hi:[1,0]
	v_pk_add_f32 v[6:7], v[6:7], 0 op_sel_hi:[1,0]
	v_pk_add_f32 v[4:5], v[4:5], v[8:9]
	v_pk_add_f32 v[6:7], v[6:7], v[10:11]
	v_cvt_f32_i32_sdwa v9, sext(v42) dst_sel:DWORD dst_unused:UNUSED_PAD src0_sel:BYTE_3
	v_cvt_f32_i32_sdwa v11, sext(v42) dst_sel:DWORD dst_unused:UNUSED_PAD src0_sel:BYTE_1
	v_cvt_f32_i32_sdwa v10, sext(v42) dst_sel:DWORD dst_unused:UNUSED_PAD src0_sel:BYTE_0
	v_cvt_f32_i32_sdwa v8, sext(v42) dst_sel:DWORD dst_unused:UNUSED_PAD src0_sel:BYTE_2
	v_pk_add_f32 v[4:5], v[4:5], v[14:15]
	v_pk_add_f32 v[6:7], v[6:7], v[16:17]
	v_pk_add_f32 v[4:5], v[4:5], v[18:19]
	v_pk_add_f32 v[6:7], v[6:7], v[20:21]
	v_pk_mul_f32 v[14:15], v[4:5], s[10:11] op_sel_hi:[1,0]
	v_pk_mul_f32 v[4:5], v[6:7], s[10:11] op_sel_hi:[1,0]
	v_pk_fma_f32 v[6:7], v[12:13], v[10:11], v[14:15] op_sel_hi:[0,1,1]
	v_pk_fma_f32 v[4:5], v[12:13], v[8:9], v[4:5] op_sel_hi:[0,1,1]
	v_cvt_f32_fp8_e32 v8, v48
	v_cvt_f32_fp8_sdwa v9, v48 src0_sel:BYTE_1
	v_cvt_f32_fp8_sdwa v10, v48 src0_sel:BYTE_2
	v_cvt_f32_fp8_sdwa v11, v48 src0_sel:BYTE_3
	v_cvt_f32_fp8_e32 v14, v49
	v_cvt_f32_fp8_sdwa v15, v49 src0_sel:BYTE_1
	v_cvt_f32_fp8_sdwa v16, v49 src0_sel:BYTE_2
	v_cvt_f32_fp8_sdwa v17, v49 src0_sel:BYTE_3
	v_cvt_f32_fp8_e32 v18, v50
	v_cvt_f32_fp8_sdwa v19, v50 src0_sel:BYTE_1
	v_cvt_f32_fp8_sdwa v20, v50 src0_sel:BYTE_2
	v_cvt_f32_fp8_sdwa v21, v50 src0_sel:BYTE_3
	v_cvt_f32_fp8_e32 v22, v51
	v_cvt_f32_fp8_sdwa v23, v51 src0_sel:BYTE_1
	v_cvt_f32_fp8_sdwa v36, v51 src0_sel:BYTE_2
	v_cvt_f32_fp8_sdwa v37, v51 src0_sel:BYTE_3
	v_pk_add_f32 v[8:9], v[8:9], 0 op_sel_hi:[1,0]
	v_pk_add_f32 v[10:11], v[10:11], 0 op_sel_hi:[1,0]
	v_pk_add_f32 v[8:9], v[8:9], v[14:15]
	v_pk_add_f32 v[10:11], v[10:11], v[16:17]
	v_cvt_f32_i32_sdwa v15, sext(v41) dst_sel:DWORD dst_unused:UNUSED_PAD src0_sel:BYTE_3
	v_cvt_f32_i32_sdwa v14, sext(v41) dst_sel:DWORD dst_unused:UNUSED_PAD src0_sel:BYTE_2
	v_pk_add_f32 v[8:9], v[8:9], v[18:19]
	v_pk_add_f32 v[10:11], v[10:11], v[20:21]
	v_cvt_f32_i32_sdwa v17, sext(v41) dst_sel:DWORD dst_unused:UNUSED_PAD src0_sel:BYTE_1
	v_cvt_f32_i32_sdwa v16, sext(v41) dst_sel:DWORD dst_unused:UNUSED_PAD src0_sel:BYTE_0
	v_pk_add_f32 v[10:11], v[10:11], v[36:37]
	v_pk_add_f32 v[8:9], v[8:9], v[22:23]
	v_cvt_f32_fp8_sdwa v20, v45 src0_sel:BYTE_2
	v_pk_mul_f32 v[18:19], v[8:9], s[10:11] op_sel_hi:[1,0]
	v_pk_mul_f32 v[8:9], v[10:11], s[10:11] op_sel_hi:[1,0]
	v_pk_fma_f32 v[10:11], v[12:13], v[16:17], v[18:19] op_sel_hi:[0,1,1]
	v_pk_fma_f32 v[8:9], v[12:13], v[14:15], v[8:9] op_sel_hi:[0,1,1]
	v_cvt_f32_fp8_e32 v14, v44
	v_cvt_f32_fp8_sdwa v15, v44 src0_sel:BYTE_1
	v_cvt_f32_fp8_sdwa v16, v44 src0_sel:BYTE_2
	v_cvt_f32_fp8_sdwa v17, v44 src0_sel:BYTE_3
	v_cvt_f32_fp8_e32 v18, v45
	v_cvt_f32_fp8_sdwa v19, v45 src0_sel:BYTE_1
	v_cvt_f32_fp8_sdwa v21, v45 src0_sel:BYTE_3
	v_cvt_f32_fp8_e32 v22, v46
	v_cvt_f32_fp8_sdwa v23, v46 src0_sel:BYTE_1
	v_cvt_f32_fp8_sdwa v36, v46 src0_sel:BYTE_2
	v_cvt_f32_fp8_sdwa v37, v46 src0_sel:BYTE_3
	v_cvt_f32_fp8_e32 v42, v47
	v_cvt_f32_fp8_sdwa v43, v47 src0_sel:BYTE_1
	v_cvt_f32_fp8_sdwa v44, v47 src0_sel:BYTE_2
	v_cvt_f32_fp8_sdwa v45, v47 src0_sel:BYTE_3
	v_pk_add_f32 v[14:15], v[14:15], 0 op_sel_hi:[1,0]
	v_pk_add_f32 v[16:17], v[16:17], 0 op_sel_hi:[1,0]
	v_pk_add_f32 v[14:15], v[14:15], v[18:19]
	v_pk_add_f32 v[16:17], v[16:17], v[20:21]
; #define GAS __attribute__((address_space(1)))
; __device__ __forceinline__ void ln_row(f32x4 (&v)[4], const GAS float* g, const GAS float* b, int lane) {
;     ...
;     for (int j = 0; j < 4; ++j) s += (v[j].x + v[j].y) + (v[j].z + v[j].w);
;     const float mean = wave_sum(s) * (1.f / D); float s2 = 0.f;
; #pragma unroll
;     for (int j = 0; j < 4; ++j) { v[j] = v[j] - mean; s2 += (v[j].x * v[j].x + v[j].y * v[j].y) + (v[j].z * v[j].z + v[j].w * v[j].w); }
;     const float rstd = __builtin_amdgcn_rsqf(wave_sum(s2) * (1.f / D) + LN_EPS);
; #pragma unroll
;     for (int j = 0; j < 4; ++j) { const f32x4 gg = *(const GAS f32x4*)(g + 4 * lane + 256 * j), bb = *(const GAS f32x4*)(b + 4 * lane + 256 * j); v[j] = v[j] * rstd * gg + bb; }
; }
; __device__ __forceinline__ void p7_combine(Frame& F, int l) {
;     ...
;             ln_row(v[r], g2, b2, lane);
;             if (lastl) store_row_f(v[r], F.H + (size_t)(m + r) * D, lane);
	v_pk_add_f32 v[14:15], v[14:15], v[22:23]
	v_cvt_f32_i32_sdwa v19, sext(v40) dst_sel:DWORD dst_unused:UNUSED_PAD src0_sel:BYTE_3
	v_cvt_f32_i32_sdwa v23, sext(v40) dst_sel:DWORD dst_unused:UNUSED_PAD src0_sel:BYTE_1
	v_cvt_f32_i32_sdwa v22, sext(v40) dst_sel:DWORD dst_unused:UNUSED_PAD src0_sel:BYTE_0
	v_cvt_f32_i32_sdwa v18, sext(v40) dst_sel:DWORD dst_unused:UNUSED_PAD src0_sel:BYTE_2
	v_pk_add_f32 v[16:17], v[16:17], v[36:37]
	v_pk_add_f32 v[14:15], v[14:15], v[42:43]
	v_pk_add_f32 v[16:17], v[16:17], v[44:45]
	v_pk_mul_f32 v[14:15], v[14:15], s[10:11] op_sel_hi:[1,0]
	v_pk_mul_f32 v[16:17], v[16:17], s[10:11] op_sel_hi:[1,0]
	v_pk_fma_f32 v[22:23], v[12:13], v[22:23], v[14:15] op_sel_hi:[0,1,1]
	v_pk_fma_f32 v[20:21], v[12:13], v[18:19], v[16:17] op_sel_hi:[0,1,1]
	v_pk_mov_b32 v[12:13], v[2:3], v[0:1] op_sel:[1,0]
	v_mov_b32_e32 v14, v2
	v_mov_b32_e32 v15, v1
	v_pk_add_f32 v[12:13], v[12:13], v[14:15]
	v_pk_mov_b32 v[14:15], v[6:7], v[4:5] op_sel:[1,0]
	v_mov_b32_e32 v16, v6
	v_mov_b32_e32 v17, v5
	v_pk_add_f32 v[14:15], v[14:15], v[16:17]
	v_add_f32_e32 v12, v12, v13
	v_pk_add_f32 v[14:15], v[14:15], v[14:15] op_sel:[0,1] op_sel_hi:[1,0]
	v_add_f32_e32 v12, 0, v12
	v_add_f32_e32 v16, v10, v11
	v_add_f32_e32 v18, v8, v9
	v_mov_b32_e32 v13, v22
	v_mov_b32_e32 v15, v23
	v_mov_b32_e32 v17, v20
	v_mov_b32_e32 v19, v21
	v_pk_add_f32 v[12:13], v[12:13], v[14:15]
	v_pk_add_f32 v[14:15], v[16:17], v[18:19]
	s_and_b64 vcc, exec, s[36:37]
	v_pk_add_f32 v[12:13], v[12:13], v[14:15]
	s_nop 0
	v_add_f32_e32 v12, v12, v13
	v_mov_b32_e32 v13, v12
	s_nop 1
	v_mov_b32_dpp v13, v13 quad_perm:[1,0,3,2] row_mask:0xf bank_mask:0xf
	v_add_f32_e32 v12, v12, v13
	v_mov_b32_e32 v13, v12
	s_nop 1
	v_mov_b32_dpp v13, v13 quad_perm:[2,3,0,1] row_mask:0xf bank_mask:0xf
	v_add_f32_e32 v12, v12, v13
	v_mov_b32_e32 v13, v12
	s_nop 1
	v_mov_b32_dpp v13, v13 row_ror:4 row_mask:0xf bank_mask:0xf
	v_add_f32_e32 v12, v12, v13
	v_mov_b32_e32 v13, v12
	s_nop 1
	v_mov_b32_dpp v13, v13 row_ror:8 row_mask:0xf bank_mask:0xf
	v_add_f32_e32 v12, v12, v13
	v_mov_b32_e32 v13, v12
	s_nop 1
	v_mov_b32_dpp v13, v13 row_bcast:15 row_mask:0xa bank_mask:0xf
	v_add_f32_e32 v12, v12, v13
	v_mov_b32_e32 v13, v12
	s_nop 1
	v_mov_b32_dpp v13, v13 row_bcast:31 row_mask:0xc bank_mask:0xf
	v_add_f32_e32 v12, v12, v13
	s_nop 0
	v_readlane_b32 s10, v12, 63
	s_nop 1
	v_fma_f32 v3, s10, v196, v3
	v_fmac_f32_e32 v2, s10, v196
	v_fma_f32 v1, s10, v196, v1
	v_fmac_f32_e32 v0, s10, v196
	v_pk_mul_f32 v[12:13], v[0:1], v[0:1]
	v_pk_mul_f32 v[14:15], v[2:3], v[2:3]
	v_fma_f32 v7, s10, v196, v7
	v_pk_mov_b32 v[16:17], v[14:15], v[12:13] op_sel:[1,0]
	v_mov_b32_e32 v15, v13
	v_pk_add_f32 v[12:13], v[16:17], v[14:15]
	v_fmac_f32_e32 v6, s10, v196
	v_fma_f32 v5, s10, v196, v5
	v_fmac_f32_e32 v4, s10, v196
	v_pk_add_f32 v[12:13], v[12:13], v[12:13] op_sel_hi:[0,1]
	v_pk_mul_f32 v[14:15], v[4:5], v[4:5]
	v_pk_mul_f32 v[16:17], v[6:7], v[6:7]
	v_fmac_f32_e32 v10, s10, v196
	v_pk_mov_b32 v[18:19], v[16:17], v[14:15] op_sel:[1,0]
	v_mov_b32_e32 v17, v15
	v_fma_f32 v11, s10, v196, v11
	v_fmac_f32_e32 v8, s10, v196
	v_mul_f32_e32 v12, v10, v10
	v_pk_add_f32 v[14:15], v[18:19], v[16:17]
	v_fma_f32 v9, s10, v196, v9
	v_pk_fma_f32 v[16:17], v[10:11], v[10:11], v[12:13] op_sel_hi:[1,1,0]
	v_mul_f32_e32 v12, v8, v8
	v_pk_add_f32 v[14:15], v[14:15], v[14:15] op_sel_hi:[0,1]
	v_pk_fma_f32 v[18:19], v[8:9], v[8:9], v[12:13] op_sel_hi:[1,1,0]
	v_fma_f32 v21, s10, v196, v21
	v_fmac_f32_e32 v20, s10, v196
	v_fma_f32 v23, s10, v196, v23
	v_fmac_f32_e32 v22, s10, v196
	v_mul_f32_e32 v16, v22, v22
	v_mul_f32_e32 v18, v23, v23
	v_mul_f32_e32 v12, v20, v20
	v_mul_f32_e32 v14, v21, v21
	v_pk_add_f32 v[16:17], v[16:17], v[18:19]
	v_pk_add_f32 v[12:13], v[12:13], v[14:15]
	s_nop 0
	v_pk_add_f32 v[12:13], v[16:17], v[12:13]
	s_nop 0
	v_add_f32_e32 v12, v12, v13
	v_mov_b32_e32 v13, v12
	s_nop 1
	v_mov_b32_dpp v13, v13 quad_perm:[1,0,3,2] row_mask:0xf bank_mask:0xf
	v_add_f32_e32 v12, v12, v13
	v_mov_b32_e32 v13, v12
	s_nop 1
	v_mov_b32_dpp v13, v13 quad_perm:[2,3,0,1] row_mask:0xf bank_mask:0xf
	v_add_f32_e32 v12, v12, v13
	v_mov_b32_e32 v13, v12
	s_nop 1
	v_mov_b32_dpp v13, v13 row_ror:4 row_mask:0xf bank_mask:0xf
	v_add_f32_e32 v12, v12, v13
	v_mov_b32_e32 v13, v12
	s_nop 1
	v_mov_b32_dpp v13, v13 row_ror:8 row_mask:0xf bank_mask:0xf
	v_add_f32_e32 v12, v12, v13
	v_mov_b32_e32 v13, v12
	s_nop 1
	v_mov_b32_dpp v13, v13 row_bcast:15 row_mask:0xa bank_mask:0xf
	v_add_f32_e32 v12, v12, v13
	v_mov_b32_e32 v13, v12
	s_nop 1
	v_mov_b32_dpp v13, v13 row_bcast:31 row_mask:0xc bank_mask:0xf
	v_add_f32_e32 v12, v12, v13
	s_nop 0
	v_readlane_b32 s10, v12, 63
	s_nop 1
	v_fma_f32 v12, s10, v197, v190
	v_rsq_f32_e32 v36, v12
	s_nop 1
	s_mov_b64 s[10:11], -1
	v_pk_mul_f32 v[40:41], v[2:3], v[36:37] op_sel_hi:[1,0]
	v_pk_mul_f32 v[0:1], v[0:1], v[36:37] op_sel_hi:[1,0]
	v_pk_mul_f32 v[4:5], v[4:5], v[36:37] op_sel_hi:[1,0]
	v_pk_mul_f32 v[8:9], v[8:9], v[36:37] op_sel_hi:[1,0]
	v_pk_mul_f32 v[22:23], v[22:23], v[36:37] op_sel_hi:[1,0]
	v_pk_mul_f32 v[20:21], v[20:21], v[36:37] op_sel_hi:[1,0]
	s_nop 0
	v_pk_fma_f32 v[2:3], v[206:207], v[0:1], v[222:223]
	v_pk_fma_f32 v[0:1], v[204:205], v[40:41], v[220:221]
	s_nop 1
	v_pk_mul_f32 v[40:41], v[6:7], v[36:37] op_sel_hi:[1,0]
	s_nop 0
	v_pk_fma_f32 v[6:7], v[210:211], v[4:5], v[226:227]
	v_pk_fma_f32 v[4:5], v[208:209], v[40:41], v[224:225]
	s_nop 1
	v_pk_mul_f32 v[40:41], v[10:11], v[36:37] op_sel_hi:[1,0]
	s_nop 0
	v_pk_fma_f32 v[10:11], v[214:215], v[8:9], v[230:231]
	v_pk_fma_f32 v[8:9], v[212:213], v[40:41], v[228:229]
	s_nop 1
	s_nop 0
	v_pk_fma_f32 v[14:15], v[20:21], v[218:219], v[234:235]
	v_pk_fma_f32 v[12:13], v[22:23], v[216:217], v[232:233]
	s_cbranch_vccnz .LBB0_1075
	v_add_co_u32_e32 v16, vcc, 0x3000, v34
	s_mov_b64 s[10:11], 0
	s_nop 0
	v_addc_co_u32_e32 v17, vcc, 0, v35, vcc
	global_store_dwordx4 v[16:17], v[0:3], off
	global_store_dwordx4 v[16:17], v[4:7], off offset:1024
	global_store_dwordx4 v[16:17], v[8:11], off offset:2048
	global_store_dwordx4 v[16:17], v[12:15], off offset:3072
